# baseline (speedup 1.0000x reference)
.LBB1_26:
	s_waitcnt vmcnt(35)
	v_and_b32_e32 v113, 3, v0
	s_and_b32 s18, s2, 15
	v_cmp_eq_u32_e32 vcc, 0, v113
	v_cmp_gt_u32_e64 s[4:5], 12, v92
	s_and_b64 s[12:13], vcc, s[4:5]
	s_lshl_b32 s4, s3, 12
	s_lshl_b32 s5, s18, 8
	s_or_b32 s4, s4, s5
	s_mul_hi_i32 s5, s4, 0x6000
	s_mulk_i32 s4, 0x6000
	s_lshl_b32 s3, s3, 8
	s_add_u32 s16, s24, s4
	s_addc_u32 s17, s25, s5
	s_ashr_i32 s4, s21, 31
	s_lshr_b32 s4, s4, 29
	s_add_i32 s4, s21, s4
	s_ashr_i32 s19, s4, 3
	v_and_b32_e32 v101, 1, v74
	v_lshl_or_b32 v74, v91, 1, v95
	s_min_i32 s4, s19, 0xff
	v_mul_u32_u24_e32 v74, 0x60, v74
	v_lshlrev_b32_e32 v75, 1, v92
	s_mul_hi_i32 s5, s4, 0x6000
	s_mulk_i32 s4, 0x6000
	v_or3_b32 v88, v74, v75, v101
	s_add_u32 s4, s16, s4
	s_addc_u32 s5, s17, s5
	v_lshlrev_b64 v[102:103], 4, v[88:89]
	v_lshl_add_u64 v[104:105], s[4:5], 0, v[102:103]
	global_load_dwordx4 v[82:85], v[104:105], off
	global_load_dwordx4 v[74:77], v[104:105], off offset:512
	global_load_dwordx4 v[78:81], v[104:105], off offset:1024
	s_waitcnt vmcnt(5)
	v_mul_f32_e32 v88, 0xbfb8aa3b, v97
	v_mul_f32_e32 v99, 0x3c91a2b4, v88
	s_waitcnt vmcnt(4)
	v_mul_f32_e32 v88, 0x4038aa3b, v96
	v_mul_f32_e32 v104, 0x3c91a2b4, v88
	v_lshrrev_b32_e32 v88, 2, v92
	v_and_b32_e32 v92, 4, v92
	v_cmp_lt_u32_e64 s[4:5], 1, v93
	v_mov_b32_e32 v93, 0xd0
	v_cmp_ne_u32_e32 vcc, 0, v92
	v_lshlrev_b32_e32 v107, 3, v88
	v_sub_u32_e32 v88, 0, v107
	v_cndmask_b32_e32 v92, 0, v93, vcc
	v_add_u32_e32 v106, v92, v86
	v_and_b32_e32 v92, 12, v0
	v_mul_u32_u24_e32 v86, 0xd0, v101
	v_mad_u32_u24 v91, v91, 24, v92
	v_mul_u32_u24_e32 v93, 12, v95
	v_lshlrev_b32_e32 v92, 20, v101
	v_add3_u32 v112, v91, v86, v93
	v_lshl_or_b32 v86, s18, 21, v90
	v_add3_u32 v86, v86, s3, v92
	v_mul_f32_e32 v1, 0xbfb8aa3b, v1
	v_and_b32_e32 v114, 24, v88
	v_or_b32_e32 v88, v86, v94
	s_min_i32 s3, s19, 0xfe
	v_mul_f32_e32 v1, 0x3c91a2b4, v1
	s_waitcnt vmcnt(3)
	v_mul_f32_e32 v105, 0x4038aa3b, v100
	v_add_u32_e32 v108, 16, v106
	v_add_u32_e32 v109, 0x70, v106
	v_add_u32_e32 v110, 0x1b0, v106
	v_add_u32_e32 v111, 0x210, v106
	v_mul_u32_u24_e32 v113, 6, v113
	s_add_i32 s19, s3, 1
	v_lshl_add_u64 v[100:101], s[16:17], 0, v[102:103]
	v_lshl_add_u64 v[102:103], v[88:89], 1, s[14:15]
	s_sub_i32 s3, 0x7ff, s21
	v_mov_b32_e32 v115, 0x7f7f7f7f
	s_mov_b32 s16, 0x42700000
	s_mov_b32 s17, 0x41f00000
	s_mov_b32 s18, 0x41700000
	v_mov_b32_e32 v116, 0x6000
	v_mov_b32_e32 v117, 0x4b400000
	v_mov_b32_e32 v118, 0x4b400008
	v_mov_b32_e32 v119, 0x4b400010
	v_mbcnt_lo_u32_b32 v200, -1, 0
	v_mbcnt_hi_u32_b32 v200, -1, v200
	v_and_b32_e32 v201, 3, v200
	v_and_b32_e32 v202, 15, v200
	v_cmp_gt_u32_e32 vcc, 8, v202
	s_nop 1
	v_cndmask_b32_e64 v178, 0, v115, vcc
	v_cndmask_b32_e64 v179, v115, 0, vcc
	v_lshlrev_b32_e32 v181, 1, v201
	v_sub_u32_e32 v202, 22, v181
	v_lshlrev_b32_e64 v180, v202, 1
	v_sub_u32_e32 v202, 16, v181
	v_lshlrev_b32_e64 v181, v202, 1
	v_lshrrev_b32_e32 v202, 3, v107
	v_sub_u32_e32 v184, v112, v202
	v_add_u32_e32 v184, v184, v201
	v_add_u32_e32 v202, 0xc0, v202
	v_cmp_eq_u32_e32 vcc, 3, v201
	s_nop 1
	v_cndmask_b32_e32 v184, v184, v202, vcc
	v_subrev_u32_e32 v185, s14, v102
	s_mov_b32 s44, s21
	s_mov_b32 s45, s22
	s_lshr_b32 s46, s44, 3
	s_add_i32 s46, s46, 1
	s_mul_i32 s46, s46, 0x6000
	s_mov_b32 s47, 0
	v_lshl_add_u64 v[196:197], v[100:101], 0, s[46:47]
	s_mov_b32 s42, 0x6000
	s_mov_b32 s43, 0
	s_sub_i32 s46, s44, 1
	s_sub_i32 s47, 0x800, s44
	s_and_b64 s[40:41], s[6:7], exec
	s_cselect_b32 s46, s46, s47
	s_cselect_b32 s41, 0, -1
	s_xor_b32 s40, s41, 0x400
	s_sub_i32 s40, s40, s41
	s_ashr_i32 s47, s46, 31
	s_lshl_b64 s[46:47], s[46:47], 10
	s_add_u32 s48, s14, s46
	s_addc_u32 s49, s15, s47
	v_readfirstlane_b32 s51, v112
	s_waitcnt vmcnt(0) lgkmcnt(0)
	v_mov_b32_e32 v176, v87
	v_rcp_f32_e32 v186, v104
	s_nop 1
	v_mul_f32_e32 v188, v105, v186
	v_mov_b32_e32 v189, 0
	v_mov_b32_e32 v190, 0
	v_mov_b32_e32 v191, 0
	s_nop 1
	s_cmp_lt_i32 s44, s45
	s_cbranch_scc0 .Lscan_exit_st
	ds_read_b64 v[122:123], v106 offset:0
	ds_read_b64 v[124:125], v106 offset:8
	ds_read_b64 v[126:127], v106 offset:16
	s_waitcnt lgkmcnt(0)
	s_cmp_lt_u32 s51, 96
	s_cbranch_scc0 .Lscan_loop_b_st
	.p2align 6
.Lscan_loop_a_st:
	ds_read_b64 v[128:129], v106 offset:96
	ds_read_b64 v[130:131], v106 offset:104
	ds_read_b64 v[132:133], v106 offset:112
	s_waitcnt vmcnt(8)
	global_load_dwordx4 v[146:149], v[196:197], off
	global_load_dwordx4 v[150:153], v[196:197], off offset:512
	global_load_dwordx4 v[154:157], v[196:197], off offset:1024
	v_lshl_add_u64 v[196:197], v[196:197], 0, s[42:43]
	s_waitcnt lgkmcnt(3)
	v_mfma_f32_16x16x128_f8f6f4 v[134:137], v[122:127], v[2:7], 0 cbsz:2 blgp:2
	v_mfma_f32_16x16x128_f8f6f4 v[138:141], v[122:127], v[14:19], 0 cbsz:2 blgp:2
	v_mfma_f32_16x16x128_f8f6f4 v[142:145], v[122:127], v[26:31], v[188:191] cbsz:2 blgp:2
	v_mfma_f32_16x16x128_f8f6f4 v[204:207], v[122:127], v[38:43], 0 cbsz:2 blgp:2
	v_mfma_f32_16x16x128_f8f6f4 v[208:211], v[122:127], v[50:55], 0 cbsz:2 blgp:2
	v_mfma_f32_16x16x128_f8f6f4 v[212:215], v[122:127], v[62:67], v[188:191] cbsz:2 blgp:2
	s_waitcnt lgkmcnt(0)
	v_mfma_f32_16x16x128_f8f6f4 v[134:137], v[128:133], v[8:13], v[134:137] cbsz:2 blgp:2
	v_mfma_f32_16x16x128_f8f6f4 v[204:207], v[128:133], v[44:49], v[204:207] cbsz:2 blgp:2
	v_mfma_f32_16x16x128_f8f6f4 v[138:141], v[128:133], v[20:25], v[138:141] cbsz:2 blgp:2
	v_mfma_f32_16x16x128_f8f6f4 v[208:211], v[128:133], v[56:61], v[208:211] cbsz:2 blgp:2
	v_mfma_f32_16x16x128_f8f6f4 v[142:145], v[128:133], v[32:37], v[142:145] cbsz:2 blgp:2
	v_mfma_f32_16x16x128_f8f6f4 v[212:215], v[128:133], v[68:73], v[212:215] cbsz:2 blgp:2
	v_cndmask_b32_e64 v158, v134, v204, s[4:5]
	v_fma_mix_f32 v158, v158, v1, v82 op_sel_hi:[0,0,1]
	v_exp_f32_e32 v158, v158
	v_cndmask_b32_e64 v159, v138, v208, s[4:5]
	v_fma_mix_f32 v159, v159, v99, v74 op_sel_hi:[0,0,1]
	v_exp_f32_e32 v159, v159
	v_fma_f32 v158, v158, v186, v186
	v_rcp_f32_e32 v158, v158
	v_add_f32_e32 v159, 1.0, v159
	v_rcp_f32_e32 v159, v159
	v_cndmask_b32_e64 v160, v142, v212, s[4:5]
	v_fma_mix_f32 v161, v158, v160, v78 op_sel_hi:[0,0,1]
	v_exp_f32_e32 v161, v161
	s_add_u32 s48, s48, s40
	v_add_f32_e32 v161, 1.0, v161
	v_rcp_f32_e32 v161, v161
	s_addc_u32 s49, s49, s41
	v_fma_f32 v162, v161, -2.0, 1.0
	v_sub_f32_e32 v163, v176, v162
	v_fma_f32 v176, v159, v163, v162
	v_fma_f32 v164, |v176|, s16, v117
	v_fma_f32 v165, |v176|, s17, v118
	v_fma_f32 v166, |v176|, s18, v119
	v_lshrrev_b32_e32 v167, 26, v176
	v_min3_u32 v164, v164, v165, v166
	v_bfi_b32 v168, 31, v164, v167
	s_nop 1
	v_mul_u32_u24_dpp v170, v168, v180 quad_perm:[1,2,3,3] row_mask:0xf bank_mask:0xf bound_ctrl:1
	v_mad_u32_u24 v171, v168, v181, v170
	ds_write_b8_d16_hi v184, v171 offset:416
	global_store_short_d16_hi v185, v176, s[48:49]
	s_waitcnt lgkmcnt(0)
	s_barrier
	ds_read_b64 v[122:123], v106 offset:416
	ds_read_b64 v[124:125], v106 offset:424
	ds_read_b64 v[126:127], v106 offset:432
	s_barrier
	ds_read_b64 v[128:129], v106 offset:512
	ds_read_b64 v[130:131], v106 offset:520
	ds_read_b64 v[132:133], v106 offset:528
	s_waitcnt lgkmcnt(3)
	v_mfma_f32_16x16x128_f8f6f4 v[134:137], v[122:127], v[2:7], 0 cbsz:2 blgp:2
	v_mfma_f32_16x16x128_f8f6f4 v[138:141], v[122:127], v[14:19], 0 cbsz:2 blgp:2
	v_mfma_f32_16x16x128_f8f6f4 v[142:145], v[122:127], v[26:31], v[188:191] cbsz:2 blgp:2
	v_mfma_f32_16x16x128_f8f6f4 v[204:207], v[122:127], v[38:43], 0 cbsz:2 blgp:2
	v_mfma_f32_16x16x128_f8f6f4 v[208:211], v[122:127], v[50:55], 0 cbsz:2 blgp:2
	v_mfma_f32_16x16x128_f8f6f4 v[212:215], v[122:127], v[62:67], v[188:191] cbsz:2 blgp:2
	s_waitcnt lgkmcnt(0)
	v_mfma_f32_16x16x128_f8f6f4 v[134:137], v[128:133], v[8:13], v[134:137] cbsz:2 blgp:2
	v_mfma_f32_16x16x128_f8f6f4 v[204:207], v[128:133], v[44:49], v[204:207] cbsz:2 blgp:2
	v_mfma_f32_16x16x128_f8f6f4 v[138:141], v[128:133], v[20:25], v[138:141] cbsz:2 blgp:2
	v_mfma_f32_16x16x128_f8f6f4 v[208:211], v[128:133], v[56:61], v[208:211] cbsz:2 blgp:2
	v_mfma_f32_16x16x128_f8f6f4 v[142:145], v[128:133], v[32:37], v[142:145] cbsz:2 blgp:2
	v_mfma_f32_16x16x128_f8f6f4 v[212:215], v[128:133], v[68:73], v[212:215] cbsz:2 blgp:2
	v_cndmask_b32_e64 v158, v134, v204, s[4:5]
	v_fma_mix_f32 v158, v158, v1, v82 op_sel:[0,0,1] op_sel_hi:[0,0,1]
	v_exp_f32_e32 v158, v158
	v_cndmask_b32_e64 v159, v138, v208, s[4:5]
	v_fma_mix_f32 v159, v159, v99, v74 op_sel:[0,0,1] op_sel_hi:[0,0,1]
	v_exp_f32_e32 v159, v159
	v_fma_f32 v158, v158, v186, v186
	v_rcp_f32_e32 v158, v158
	v_add_f32_e32 v159, 1.0, v159
	v_rcp_f32_e32 v159, v159
	v_cndmask_b32_e64 v160, v142, v212, s[4:5]
	v_fma_mix_f32 v161, v158, v160, v78 op_sel:[0,0,1] op_sel_hi:[0,0,1]
	v_exp_f32_e32 v161, v161
	s_add_u32 s48, s48, s40
	v_add_f32_e32 v161, 1.0, v161
	v_rcp_f32_e32 v161, v161
	s_addc_u32 s49, s49, s41
	v_fma_f32 v162, v161, -2.0, 1.0
	v_sub_f32_e32 v163, v176, v162
	v_fma_f32 v176, v159, v163, v162
	v_fma_f32 v164, |v176|, s16, v117
	v_fma_f32 v165, |v176|, s17, v118
	v_fma_f32 v166, |v176|, s18, v119
	v_lshrrev_b32_e32 v167, 26, v176
	v_min3_u32 v164, v164, v165, v166
	v_bfi_b32 v168, 31, v164, v167
	s_nop 1
	v_mul_u32_u24_dpp v170, v168, v180 quad_perm:[1,2,3,3] row_mask:0xf bank_mask:0xf bound_ctrl:1
	v_mad_u32_u24 v171, v168, v181, v170
	ds_write_b8_d16_hi v184, v171
	global_store_short_d16_hi v185, v176, s[48:49]
	s_waitcnt lgkmcnt(0)
	s_barrier
	ds_read_b64 v[122:123], v106 offset:0
	ds_read_b64 v[124:125], v106 offset:8
	ds_read_b64 v[126:127], v106 offset:16
	s_barrier
	ds_read_b64 v[128:129], v106 offset:96
	ds_read_b64 v[130:131], v106 offset:104
	ds_read_b64 v[132:133], v106 offset:112
	s_waitcnt lgkmcnt(3)
	v_mfma_f32_16x16x128_f8f6f4 v[134:137], v[122:127], v[2:7], 0 cbsz:2 blgp:2
	v_mfma_f32_16x16x128_f8f6f4 v[138:141], v[122:127], v[14:19], 0 cbsz:2 blgp:2
	v_mfma_f32_16x16x128_f8f6f4 v[142:145], v[122:127], v[26:31], v[188:191] cbsz:2 blgp:2
	v_mfma_f32_16x16x128_f8f6f4 v[204:207], v[122:127], v[38:43], 0 cbsz:2 blgp:2
	v_mfma_f32_16x16x128_f8f6f4 v[208:211], v[122:127], v[50:55], 0 cbsz:2 blgp:2
	v_mfma_f32_16x16x128_f8f6f4 v[212:215], v[122:127], v[62:67], v[188:191] cbsz:2 blgp:2
	s_waitcnt lgkmcnt(0)
	v_mfma_f32_16x16x128_f8f6f4 v[134:137], v[128:133], v[8:13], v[134:137] cbsz:2 blgp:2
	v_mfma_f32_16x16x128_f8f6f4 v[204:207], v[128:133], v[44:49], v[204:207] cbsz:2 blgp:2
	v_mfma_f32_16x16x128_f8f6f4 v[138:141], v[128:133], v[20:25], v[138:141] cbsz:2 blgp:2
	v_mfma_f32_16x16x128_f8f6f4 v[208:211], v[128:133], v[56:61], v[208:211] cbsz:2 blgp:2
	v_mfma_f32_16x16x128_f8f6f4 v[142:145], v[128:133], v[32:37], v[142:145] cbsz:2 blgp:2
	v_mfma_f32_16x16x128_f8f6f4 v[212:215], v[128:133], v[68:73], v[212:215] cbsz:2 blgp:2
	v_cndmask_b32_e64 v158, v134, v204, s[4:5]
	v_fma_mix_f32 v158, v158, v1, v83 op_sel_hi:[0,0,1]
	v_exp_f32_e32 v158, v158
	v_cndmask_b32_e64 v159, v138, v208, s[4:5]
	v_fma_mix_f32 v159, v159, v99, v75 op_sel_hi:[0,0,1]
	v_exp_f32_e32 v159, v159
	v_fma_f32 v158, v158, v186, v186
	v_rcp_f32_e32 v158, v158
	v_add_f32_e32 v159, 1.0, v159
	v_rcp_f32_e32 v159, v159
	v_cndmask_b32_e64 v160, v142, v212, s[4:5]
	v_fma_mix_f32 v161, v158, v160, v79 op_sel_hi:[0,0,1]
	v_exp_f32_e32 v161, v161
	s_add_u32 s48, s48, s40
	v_add_f32_e32 v161, 1.0, v161
	v_rcp_f32_e32 v161, v161
	s_addc_u32 s49, s49, s41
	v_fma_f32 v162, v161, -2.0, 1.0
	v_sub_f32_e32 v163, v176, v162
	v_fma_f32 v176, v159, v163, v162
	v_fma_f32 v164, |v176|, s16, v117
	v_fma_f32 v165, |v176|, s17, v118
	v_fma_f32 v166, |v176|, s18, v119
	v_lshrrev_b32_e32 v167, 26, v176
	v_min3_u32 v164, v164, v165, v166
	v_bfi_b32 v168, 31, v164, v167
	s_nop 1
	v_mul_u32_u24_dpp v170, v168, v180 quad_perm:[1,2,3,3] row_mask:0xf bank_mask:0xf bound_ctrl:1
	v_mad_u32_u24 v171, v168, v181, v170
	ds_write_b8_d16_hi v184, v171 offset:416
	global_store_short_d16_hi v185, v176, s[48:49]
	s_waitcnt lgkmcnt(0)
	s_barrier
	ds_read_b64 v[122:123], v106 offset:416
	ds_read_b64 v[124:125], v106 offset:424
	ds_read_b64 v[126:127], v106 offset:432
	s_barrier
	ds_read_b64 v[128:129], v106 offset:512
	ds_read_b64 v[130:131], v106 offset:520
	ds_read_b64 v[132:133], v106 offset:528
	s_waitcnt lgkmcnt(3)
	v_mfma_f32_16x16x128_f8f6f4 v[134:137], v[122:127], v[2:7], 0 cbsz:2 blgp:2
	v_mfma_f32_16x16x128_f8f6f4 v[138:141], v[122:127], v[14:19], 0 cbsz:2 blgp:2
	v_mfma_f32_16x16x128_f8f6f4 v[142:145], v[122:127], v[26:31], v[188:191] cbsz:2 blgp:2
	v_mfma_f32_16x16x128_f8f6f4 v[204:207], v[122:127], v[38:43], 0 cbsz:2 blgp:2
	v_mfma_f32_16x16x128_f8f6f4 v[208:211], v[122:127], v[50:55], 0 cbsz:2 blgp:2
	v_mfma_f32_16x16x128_f8f6f4 v[212:215], v[122:127], v[62:67], v[188:191] cbsz:2 blgp:2
	s_waitcnt lgkmcnt(0)
	v_mfma_f32_16x16x128_f8f6f4 v[134:137], v[128:133], v[8:13], v[134:137] cbsz:2 blgp:2
	v_mfma_f32_16x16x128_f8f6f4 v[204:207], v[128:133], v[44:49], v[204:207] cbsz:2 blgp:2
	v_mfma_f32_16x16x128_f8f6f4 v[138:141], v[128:133], v[20:25], v[138:141] cbsz:2 blgp:2
	v_mfma_f32_16x16x128_f8f6f4 v[208:211], v[128:133], v[56:61], v[208:211] cbsz:2 blgp:2
	v_mfma_f32_16x16x128_f8f6f4 v[142:145], v[128:133], v[32:37], v[142:145] cbsz:2 blgp:2
	v_mfma_f32_16x16x128_f8f6f4 v[212:215], v[128:133], v[68:73], v[212:215] cbsz:2 blgp:2
	v_cndmask_b32_e64 v158, v134, v204, s[4:5]
	v_fma_mix_f32 v158, v158, v1, v83 op_sel:[0,0,1] op_sel_hi:[0,0,1]
	v_exp_f32_e32 v158, v158
	v_cndmask_b32_e64 v159, v138, v208, s[4:5]
	v_fma_mix_f32 v159, v159, v99, v75 op_sel:[0,0,1] op_sel_hi:[0,0,1]
	v_exp_f32_e32 v159, v159
	v_fma_f32 v158, v158, v186, v186
	v_rcp_f32_e32 v158, v158
	v_add_f32_e32 v159, 1.0, v159
	v_rcp_f32_e32 v159, v159
	v_cndmask_b32_e64 v160, v142, v212, s[4:5]
	v_fma_mix_f32 v161, v158, v160, v79 op_sel:[0,0,1] op_sel_hi:[0,0,1]
	v_exp_f32_e32 v161, v161
	s_add_u32 s48, s48, s40
	v_add_f32_e32 v161, 1.0, v161
	v_rcp_f32_e32 v161, v161
	s_addc_u32 s49, s49, s41
	v_fma_f32 v162, v161, -2.0, 1.0
	v_sub_f32_e32 v163, v176, v162
	v_fma_f32 v176, v159, v163, v162
	v_fma_f32 v164, |v176|, s16, v117
	v_fma_f32 v165, |v176|, s17, v118
	v_fma_f32 v166, |v176|, s18, v119
	v_lshrrev_b32_e32 v167, 26, v176
	v_min3_u32 v164, v164, v165, v166
	v_bfi_b32 v168, 31, v164, v167
	s_nop 1
	v_mul_u32_u24_dpp v170, v168, v180 quad_perm:[1,2,3,3] row_mask:0xf bank_mask:0xf bound_ctrl:1
	v_mad_u32_u24 v171, v168, v181, v170
	ds_write_b8_d16_hi v184, v171
	global_store_short_d16_hi v185, v176, s[48:49]
	s_waitcnt lgkmcnt(0)
	s_barrier
	ds_read_b64 v[122:123], v106 offset:0
	ds_read_b64 v[124:125], v106 offset:8
	ds_read_b64 v[126:127], v106 offset:16
	s_barrier
	ds_read_b64 v[128:129], v106 offset:96
	ds_read_b64 v[130:131], v106 offset:104
	ds_read_b64 v[132:133], v106 offset:112
	s_waitcnt lgkmcnt(3)
	v_mfma_f32_16x16x128_f8f6f4 v[134:137], v[122:127], v[2:7], 0 cbsz:2 blgp:2
	v_mfma_f32_16x16x128_f8f6f4 v[138:141], v[122:127], v[14:19], 0 cbsz:2 blgp:2
	v_mfma_f32_16x16x128_f8f6f4 v[142:145], v[122:127], v[26:31], v[188:191] cbsz:2 blgp:2
	v_mfma_f32_16x16x128_f8f6f4 v[204:207], v[122:127], v[38:43], 0 cbsz:2 blgp:2
	v_mfma_f32_16x16x128_f8f6f4 v[208:211], v[122:127], v[50:55], 0 cbsz:2 blgp:2
	v_mfma_f32_16x16x128_f8f6f4 v[212:215], v[122:127], v[62:67], v[188:191] cbsz:2 blgp:2
	s_waitcnt lgkmcnt(0)
	v_mfma_f32_16x16x128_f8f6f4 v[134:137], v[128:133], v[8:13], v[134:137] cbsz:2 blgp:2
	v_mfma_f32_16x16x128_f8f6f4 v[204:207], v[128:133], v[44:49], v[204:207] cbsz:2 blgp:2
	v_mfma_f32_16x16x128_f8f6f4 v[138:141], v[128:133], v[20:25], v[138:141] cbsz:2 blgp:2
	v_mfma_f32_16x16x128_f8f6f4 v[208:211], v[128:133], v[56:61], v[208:211] cbsz:2 blgp:2
	v_mfma_f32_16x16x128_f8f6f4 v[142:145], v[128:133], v[32:37], v[142:145] cbsz:2 blgp:2
	v_mfma_f32_16x16x128_f8f6f4 v[212:215], v[128:133], v[68:73], v[212:215] cbsz:2 blgp:2
	v_cndmask_b32_e64 v158, v134, v204, s[4:5]
	v_fma_mix_f32 v158, v158, v1, v84 op_sel_hi:[0,0,1]
	v_exp_f32_e32 v158, v158
	v_cndmask_b32_e64 v159, v138, v208, s[4:5]
	v_fma_mix_f32 v159, v159, v99, v76 op_sel_hi:[0,0,1]
	v_exp_f32_e32 v159, v159
	v_fma_f32 v158, v158, v186, v186
	v_rcp_f32_e32 v158, v158
	v_add_f32_e32 v159, 1.0, v159
	v_rcp_f32_e32 v159, v159
	v_cndmask_b32_e64 v160, v142, v212, s[4:5]
	v_fma_mix_f32 v161, v158, v160, v80 op_sel_hi:[0,0,1]
	v_exp_f32_e32 v161, v161
	s_add_u32 s48, s48, s40
	v_add_f32_e32 v161, 1.0, v161
	v_rcp_f32_e32 v161, v161
	s_addc_u32 s49, s49, s41
	v_fma_f32 v162, v161, -2.0, 1.0
	v_sub_f32_e32 v163, v176, v162
	v_fma_f32 v176, v159, v163, v162
	v_fma_f32 v164, |v176|, s16, v117
	v_fma_f32 v165, |v176|, s17, v118
	v_fma_f32 v166, |v176|, s18, v119
	v_lshrrev_b32_e32 v167, 26, v176
	v_min3_u32 v164, v164, v165, v166
	v_bfi_b32 v168, 31, v164, v167
	s_nop 1
	v_mul_u32_u24_dpp v170, v168, v180 quad_perm:[1,2,3,3] row_mask:0xf bank_mask:0xf bound_ctrl:1
	v_mad_u32_u24 v171, v168, v181, v170
	ds_write_b8_d16_hi v184, v171 offset:416
	global_store_short_d16_hi v185, v176, s[48:49]
	s_waitcnt lgkmcnt(0)
	s_barrier
	ds_read_b64 v[122:123], v106 offset:416
	ds_read_b64 v[124:125], v106 offset:424
	ds_read_b64 v[126:127], v106 offset:432
	s_barrier
	ds_read_b64 v[128:129], v106 offset:512
	ds_read_b64 v[130:131], v106 offset:520
	ds_read_b64 v[132:133], v106 offset:528
	s_waitcnt lgkmcnt(3)
	v_mfma_f32_16x16x128_f8f6f4 v[134:137], v[122:127], v[2:7], 0 cbsz:2 blgp:2
	v_mfma_f32_16x16x128_f8f6f4 v[138:141], v[122:127], v[14:19], 0 cbsz:2 blgp:2
	v_mfma_f32_16x16x128_f8f6f4 v[142:145], v[122:127], v[26:31], v[188:191] cbsz:2 blgp:2
	v_mfma_f32_16x16x128_f8f6f4 v[204:207], v[122:127], v[38:43], 0 cbsz:2 blgp:2
	v_mfma_f32_16x16x128_f8f6f4 v[208:211], v[122:127], v[50:55], 0 cbsz:2 blgp:2
	v_mfma_f32_16x16x128_f8f6f4 v[212:215], v[122:127], v[62:67], v[188:191] cbsz:2 blgp:2
	s_waitcnt lgkmcnt(0)
	v_mfma_f32_16x16x128_f8f6f4 v[134:137], v[128:133], v[8:13], v[134:137] cbsz:2 blgp:2
	v_mfma_f32_16x16x128_f8f6f4 v[204:207], v[128:133], v[44:49], v[204:207] cbsz:2 blgp:2
	v_mfma_f32_16x16x128_f8f6f4 v[138:141], v[128:133], v[20:25], v[138:141] cbsz:2 blgp:2
	v_mfma_f32_16x16x128_f8f6f4 v[208:211], v[128:133], v[56:61], v[208:211] cbsz:2 blgp:2
	v_mfma_f32_16x16x128_f8f6f4 v[142:145], v[128:133], v[32:37], v[142:145] cbsz:2 blgp:2
	v_mfma_f32_16x16x128_f8f6f4 v[212:215], v[128:133], v[68:73], v[212:215] cbsz:2 blgp:2
	v_cndmask_b32_e64 v158, v134, v204, s[4:5]
	v_fma_mix_f32 v158, v158, v1, v84 op_sel:[0,0,1] op_sel_hi:[0,0,1]
	v_exp_f32_e32 v158, v158
	v_cndmask_b32_e64 v159, v138, v208, s[4:5]
	v_fma_mix_f32 v159, v159, v99, v76 op_sel:[0,0,1] op_sel_hi:[0,0,1]
	v_exp_f32_e32 v159, v159
	v_fma_f32 v158, v158, v186, v186
	v_rcp_f32_e32 v158, v158
	v_add_f32_e32 v159, 1.0, v159
	v_rcp_f32_e32 v159, v159
	v_cndmask_b32_e64 v160, v142, v212, s[4:5]
	v_fma_mix_f32 v161, v158, v160, v80 op_sel:[0,0,1] op_sel_hi:[0,0,1]
	v_exp_f32_e32 v161, v161
	s_add_u32 s48, s48, s40
	v_add_f32_e32 v161, 1.0, v161
	v_rcp_f32_e32 v161, v161
	s_addc_u32 s49, s49, s41
	v_fma_f32 v162, v161, -2.0, 1.0
	v_sub_f32_e32 v163, v176, v162
	v_fma_f32 v176, v159, v163, v162
	v_fma_f32 v164, |v176|, s16, v117
	v_fma_f32 v165, |v176|, s17, v118
	v_fma_f32 v166, |v176|, s18, v119
	v_lshrrev_b32_e32 v167, 26, v176
	v_min3_u32 v164, v164, v165, v166
	v_bfi_b32 v168, 31, v164, v167
	s_nop 1
	v_mul_u32_u24_dpp v170, v168, v180 quad_perm:[1,2,3,3] row_mask:0xf bank_mask:0xf bound_ctrl:1
	v_mad_u32_u24 v171, v168, v181, v170
	ds_write_b8_d16_hi v184, v171
	global_store_short_d16_hi v185, v176, s[48:49]
	s_waitcnt lgkmcnt(0)
	s_barrier
	ds_read_b64 v[122:123], v106 offset:0
	ds_read_b64 v[124:125], v106 offset:8
	ds_read_b64 v[126:127], v106 offset:16
	s_barrier
	ds_read_b64 v[128:129], v106 offset:96
	ds_read_b64 v[130:131], v106 offset:104
	ds_read_b64 v[132:133], v106 offset:112
	s_waitcnt lgkmcnt(3)
	v_mfma_f32_16x16x128_f8f6f4 v[134:137], v[122:127], v[2:7], 0 cbsz:2 blgp:2
	v_mfma_f32_16x16x128_f8f6f4 v[138:141], v[122:127], v[14:19], 0 cbsz:2 blgp:2
	v_mfma_f32_16x16x128_f8f6f4 v[142:145], v[122:127], v[26:31], v[188:191] cbsz:2 blgp:2
	v_mfma_f32_16x16x128_f8f6f4 v[204:207], v[122:127], v[38:43], 0 cbsz:2 blgp:2
	v_mfma_f32_16x16x128_f8f6f4 v[208:211], v[122:127], v[50:55], 0 cbsz:2 blgp:2
	v_mfma_f32_16x16x128_f8f6f4 v[212:215], v[122:127], v[62:67], v[188:191] cbsz:2 blgp:2
	s_waitcnt lgkmcnt(0)
	v_mfma_f32_16x16x128_f8f6f4 v[134:137], v[128:133], v[8:13], v[134:137] cbsz:2 blgp:2
	v_mfma_f32_16x16x128_f8f6f4 v[204:207], v[128:133], v[44:49], v[204:207] cbsz:2 blgp:2
	v_mfma_f32_16x16x128_f8f6f4 v[138:141], v[128:133], v[20:25], v[138:141] cbsz:2 blgp:2
	v_mfma_f32_16x16x128_f8f6f4 v[208:211], v[128:133], v[56:61], v[208:211] cbsz:2 blgp:2
	v_mfma_f32_16x16x128_f8f6f4 v[142:145], v[128:133], v[32:37], v[142:145] cbsz:2 blgp:2
	v_mfma_f32_16x16x128_f8f6f4 v[212:215], v[128:133], v[68:73], v[212:215] cbsz:2 blgp:2
	v_cndmask_b32_e64 v158, v134, v204, s[4:5]
	v_fma_mix_f32 v158, v158, v1, v85 op_sel_hi:[0,0,1]
	v_exp_f32_e32 v158, v158
	v_cndmask_b32_e64 v159, v138, v208, s[4:5]
	v_fma_mix_f32 v159, v159, v99, v77 op_sel_hi:[0,0,1]
	v_exp_f32_e32 v159, v159
	v_fma_f32 v158, v158, v186, v186
	v_rcp_f32_e32 v158, v158
	v_add_f32_e32 v159, 1.0, v159
	v_rcp_f32_e32 v159, v159
	v_cndmask_b32_e64 v160, v142, v212, s[4:5]
	v_fma_mix_f32 v161, v158, v160, v81 op_sel_hi:[0,0,1]
	v_exp_f32_e32 v161, v161
	s_add_u32 s48, s48, s40
	v_add_f32_e32 v161, 1.0, v161
	v_rcp_f32_e32 v161, v161
	s_addc_u32 s49, s49, s41
	v_fma_f32 v162, v161, -2.0, 1.0
	v_sub_f32_e32 v163, v176, v162
	v_fma_f32 v176, v159, v163, v162
	v_fma_f32 v164, |v176|, s16, v117
	v_fma_f32 v165, |v176|, s17, v118
	v_fma_f32 v166, |v176|, s18, v119
	v_lshrrev_b32_e32 v167, 26, v176
	v_min3_u32 v164, v164, v165, v166
	v_bfi_b32 v168, 31, v164, v167
	s_nop 1
	v_mul_u32_u24_dpp v170, v168, v180 quad_perm:[1,2,3,3] row_mask:0xf bank_mask:0xf bound_ctrl:1
	v_mad_u32_u24 v171, v168, v181, v170
	ds_write_b8_d16_hi v184, v171 offset:416
	global_store_short_d16_hi v185, v176, s[48:49]
	s_waitcnt lgkmcnt(0)
	s_barrier
	ds_read_b64 v[122:123], v106 offset:416
	ds_read_b64 v[124:125], v106 offset:424
	ds_read_b64 v[126:127], v106 offset:432
	s_barrier
	ds_read_b64 v[128:129], v106 offset:512
	ds_read_b64 v[130:131], v106 offset:520
	ds_read_b64 v[132:133], v106 offset:528
	s_waitcnt lgkmcnt(3)
	v_mfma_f32_16x16x128_f8f6f4 v[134:137], v[122:127], v[2:7], 0 cbsz:2 blgp:2
	v_mfma_f32_16x16x128_f8f6f4 v[138:141], v[122:127], v[14:19], 0 cbsz:2 blgp:2
	v_mfma_f32_16x16x128_f8f6f4 v[142:145], v[122:127], v[26:31], v[188:191] cbsz:2 blgp:2
	v_mfma_f32_16x16x128_f8f6f4 v[204:207], v[122:127], v[38:43], 0 cbsz:2 blgp:2
	v_mfma_f32_16x16x128_f8f6f4 v[208:211], v[122:127], v[50:55], 0 cbsz:2 blgp:2
	v_mfma_f32_16x16x128_f8f6f4 v[212:215], v[122:127], v[62:67], v[188:191] cbsz:2 blgp:2
	s_waitcnt lgkmcnt(0)
	v_mfma_f32_16x16x128_f8f6f4 v[134:137], v[128:133], v[8:13], v[134:137] cbsz:2 blgp:2
	v_mfma_f32_16x16x128_f8f6f4 v[204:207], v[128:133], v[44:49], v[204:207] cbsz:2 blgp:2
	v_mfma_f32_16x16x128_f8f6f4 v[138:141], v[128:133], v[20:25], v[138:141] cbsz:2 blgp:2
	v_mfma_f32_16x16x128_f8f6f4 v[208:211], v[128:133], v[56:61], v[208:211] cbsz:2 blgp:2
	v_mfma_f32_16x16x128_f8f6f4 v[142:145], v[128:133], v[32:37], v[142:145] cbsz:2 blgp:2
	v_mfma_f32_16x16x128_f8f6f4 v[212:215], v[128:133], v[68:73], v[212:215] cbsz:2 blgp:2
	v_cndmask_b32_e64 v158, v134, v204, s[4:5]
	v_fma_mix_f32 v158, v158, v1, v85 op_sel:[0,0,1] op_sel_hi:[0,0,1]
	v_exp_f32_e32 v158, v158
	v_cndmask_b32_e64 v159, v138, v208, s[4:5]
	v_fma_mix_f32 v159, v159, v99, v77 op_sel:[0,0,1] op_sel_hi:[0,0,1]
	v_exp_f32_e32 v159, v159
	v_fma_f32 v158, v158, v186, v186
	v_rcp_f32_e32 v158, v158
	v_add_f32_e32 v159, 1.0, v159
	v_rcp_f32_e32 v159, v159
	v_cndmask_b32_e64 v160, v142, v212, s[4:5]
	v_fma_mix_f32 v161, v158, v160, v81 op_sel:[0,0,1] op_sel_hi:[0,0,1]
	v_exp_f32_e32 v161, v161
	s_add_u32 s48, s48, s40
	v_add_f32_e32 v161, 1.0, v161
	v_rcp_f32_e32 v161, v161
	s_addc_u32 s49, s49, s41
	v_fma_f32 v162, v161, -2.0, 1.0
	v_sub_f32_e32 v163, v176, v162
	v_fma_f32 v176, v159, v163, v162
	v_fma_f32 v164, |v176|, s16, v117
	v_fma_f32 v165, |v176|, s17, v118
	v_fma_f32 v166, |v176|, s18, v119
	v_lshrrev_b32_e32 v167, 26, v176
	v_min3_u32 v164, v164, v165, v166
	v_bfi_b32 v168, 31, v164, v167
	s_nop 1
	v_mul_u32_u24_dpp v170, v168, v180 quad_perm:[1,2,3,3] row_mask:0xf bank_mask:0xf bound_ctrl:1
	v_mad_u32_u24 v171, v168, v181, v170
	ds_write_b8_d16_hi v184, v171
	global_store_short_d16_hi v185, v176, s[48:49]
	s_waitcnt lgkmcnt(0)
	s_barrier
	ds_read_b64 v[122:123], v106 offset:0
	ds_read_b64 v[124:125], v106 offset:8
	ds_read_b64 v[126:127], v106 offset:16
	s_barrier
	ds_read_b64 v[128:129], v106 offset:96
	ds_read_b64 v[130:131], v106 offset:104
	ds_read_b64 v[132:133], v106 offset:112
	s_waitcnt vmcnt(8)
	global_load_dwordx4 v[82:85], v[196:197], off
	global_load_dwordx4 v[74:77], v[196:197], off offset:512
	global_load_dwordx4 v[78:81], v[196:197], off offset:1024
	v_lshl_add_u64 v[196:197], v[196:197], 0, s[42:43]
	s_waitcnt lgkmcnt(3)
	v_mfma_f32_16x16x128_f8f6f4 v[134:137], v[122:127], v[2:7], 0 cbsz:2 blgp:2
	v_mfma_f32_16x16x128_f8f6f4 v[138:141], v[122:127], v[14:19], 0 cbsz:2 blgp:2
	v_mfma_f32_16x16x128_f8f6f4 v[142:145], v[122:127], v[26:31], v[188:191] cbsz:2 blgp:2
	v_mfma_f32_16x16x128_f8f6f4 v[204:207], v[122:127], v[38:43], 0 cbsz:2 blgp:2
	v_mfma_f32_16x16x128_f8f6f4 v[208:211], v[122:127], v[50:55], 0 cbsz:2 blgp:2
	v_mfma_f32_16x16x128_f8f6f4 v[212:215], v[122:127], v[62:67], v[188:191] cbsz:2 blgp:2
	s_waitcnt lgkmcnt(0)
	v_mfma_f32_16x16x128_f8f6f4 v[134:137], v[128:133], v[8:13], v[134:137] cbsz:2 blgp:2
	v_mfma_f32_16x16x128_f8f6f4 v[204:207], v[128:133], v[44:49], v[204:207] cbsz:2 blgp:2
	v_mfma_f32_16x16x128_f8f6f4 v[138:141], v[128:133], v[20:25], v[138:141] cbsz:2 blgp:2
	v_mfma_f32_16x16x128_f8f6f4 v[208:211], v[128:133], v[56:61], v[208:211] cbsz:2 blgp:2
	v_mfma_f32_16x16x128_f8f6f4 v[142:145], v[128:133], v[32:37], v[142:145] cbsz:2 blgp:2
	v_mfma_f32_16x16x128_f8f6f4 v[212:215], v[128:133], v[68:73], v[212:215] cbsz:2 blgp:2
	v_cndmask_b32_e64 v158, v134, v204, s[4:5]
	v_fma_mix_f32 v158, v158, v1, v146 op_sel_hi:[0,0,1]
	v_exp_f32_e32 v158, v158
	v_cndmask_b32_e64 v159, v138, v208, s[4:5]
	v_fma_mix_f32 v159, v159, v99, v150 op_sel_hi:[0,0,1]
	v_exp_f32_e32 v159, v159
	v_fma_f32 v158, v158, v186, v186
	v_rcp_f32_e32 v158, v158
	v_add_f32_e32 v159, 1.0, v159
	v_rcp_f32_e32 v159, v159
	v_cndmask_b32_e64 v160, v142, v212, s[4:5]
	v_fma_mix_f32 v161, v158, v160, v154 op_sel_hi:[0,0,1]
	v_exp_f32_e32 v161, v161
	s_add_u32 s48, s48, s40
	v_add_f32_e32 v161, 1.0, v161
	v_rcp_f32_e32 v161, v161
	s_addc_u32 s49, s49, s41
	v_fma_f32 v162, v161, -2.0, 1.0
	v_sub_f32_e32 v163, v176, v162
	v_fma_f32 v176, v159, v163, v162
	v_fma_f32 v164, |v176|, s16, v117
	v_fma_f32 v165, |v176|, s17, v118
	v_fma_f32 v166, |v176|, s18, v119
	v_lshrrev_b32_e32 v167, 26, v176
	v_min3_u32 v164, v164, v165, v166
	v_bfi_b32 v168, 31, v164, v167
	s_nop 1
	v_mul_u32_u24_dpp v170, v168, v180 quad_perm:[1,2,3,3] row_mask:0xf bank_mask:0xf bound_ctrl:1
	v_mad_u32_u24 v171, v168, v181, v170
	ds_write_b8_d16_hi v184, v171 offset:416
	global_store_short_d16_hi v185, v176, s[48:49]
	s_waitcnt lgkmcnt(0)
	s_barrier
	ds_read_b64 v[122:123], v106 offset:416
	ds_read_b64 v[124:125], v106 offset:424
	ds_read_b64 v[126:127], v106 offset:432
	s_barrier
	ds_read_b64 v[128:129], v106 offset:512
	ds_read_b64 v[130:131], v106 offset:520
	ds_read_b64 v[132:133], v106 offset:528
	s_waitcnt lgkmcnt(3)
	v_mfma_f32_16x16x128_f8f6f4 v[134:137], v[122:127], v[2:7], 0 cbsz:2 blgp:2
	v_mfma_f32_16x16x128_f8f6f4 v[138:141], v[122:127], v[14:19], 0 cbsz:2 blgp:2
	v_mfma_f32_16x16x128_f8f6f4 v[142:145], v[122:127], v[26:31], v[188:191] cbsz:2 blgp:2
	v_mfma_f32_16x16x128_f8f6f4 v[204:207], v[122:127], v[38:43], 0 cbsz:2 blgp:2
	v_mfma_f32_16x16x128_f8f6f4 v[208:211], v[122:127], v[50:55], 0 cbsz:2 blgp:2
	v_mfma_f32_16x16x128_f8f6f4 v[212:215], v[122:127], v[62:67], v[188:191] cbsz:2 blgp:2
	s_waitcnt lgkmcnt(0)
	v_mfma_f32_16x16x128_f8f6f4 v[134:137], v[128:133], v[8:13], v[134:137] cbsz:2 blgp:2
	v_mfma_f32_16x16x128_f8f6f4 v[204:207], v[128:133], v[44:49], v[204:207] cbsz:2 blgp:2
	v_mfma_f32_16x16x128_f8f6f4 v[138:141], v[128:133], v[20:25], v[138:141] cbsz:2 blgp:2
	v_mfma_f32_16x16x128_f8f6f4 v[208:211], v[128:133], v[56:61], v[208:211] cbsz:2 blgp:2
	v_mfma_f32_16x16x128_f8f6f4 v[142:145], v[128:133], v[32:37], v[142:145] cbsz:2 blgp:2
	v_mfma_f32_16x16x128_f8f6f4 v[212:215], v[128:133], v[68:73], v[212:215] cbsz:2 blgp:2
	v_cndmask_b32_e64 v158, v134, v204, s[4:5]
	v_fma_mix_f32 v158, v158, v1, v146 op_sel:[0,0,1] op_sel_hi:[0,0,1]
	v_exp_f32_e32 v158, v158
	v_cndmask_b32_e64 v159, v138, v208, s[4:5]
	v_fma_mix_f32 v159, v159, v99, v150 op_sel:[0,0,1] op_sel_hi:[0,0,1]
	v_exp_f32_e32 v159, v159
	v_fma_f32 v158, v158, v186, v186
	v_rcp_f32_e32 v158, v158
	v_add_f32_e32 v159, 1.0, v159
	v_rcp_f32_e32 v159, v159
	v_cndmask_b32_e64 v160, v142, v212, s[4:5]
	v_fma_mix_f32 v161, v158, v160, v154 op_sel:[0,0,1] op_sel_hi:[0,0,1]
	v_exp_f32_e32 v161, v161
	s_add_u32 s48, s48, s40
	v_add_f32_e32 v161, 1.0, v161
	v_rcp_f32_e32 v161, v161
	s_addc_u32 s49, s49, s41
	v_fma_f32 v162, v161, -2.0, 1.0
	v_sub_f32_e32 v163, v176, v162
	v_fma_f32 v176, v159, v163, v162
	v_fma_f32 v164, |v176|, s16, v117
	v_fma_f32 v165, |v176|, s17, v118
	v_fma_f32 v166, |v176|, s18, v119
	v_lshrrev_b32_e32 v167, 26, v176
	v_min3_u32 v164, v164, v165, v166
	v_bfi_b32 v168, 31, v164, v167
	s_nop 1
	v_mul_u32_u24_dpp v170, v168, v180 quad_perm:[1,2,3,3] row_mask:0xf bank_mask:0xf bound_ctrl:1
	v_mad_u32_u24 v171, v168, v181, v170
	ds_write_b8_d16_hi v184, v171
	global_store_short_d16_hi v185, v176, s[48:49]
	s_waitcnt lgkmcnt(0)
	s_barrier
	ds_read_b64 v[122:123], v106 offset:0
	ds_read_b64 v[124:125], v106 offset:8
	ds_read_b64 v[126:127], v106 offset:16
	s_barrier
	ds_read_b64 v[128:129], v106 offset:96
	ds_read_b64 v[130:131], v106 offset:104
	ds_read_b64 v[132:133], v106 offset:112
	s_waitcnt lgkmcnt(3)
	v_mfma_f32_16x16x128_f8f6f4 v[134:137], v[122:127], v[2:7], 0 cbsz:2 blgp:2
	v_mfma_f32_16x16x128_f8f6f4 v[138:141], v[122:127], v[14:19], 0 cbsz:2 blgp:2
	v_mfma_f32_16x16x128_f8f6f4 v[142:145], v[122:127], v[26:31], v[188:191] cbsz:2 blgp:2
	v_mfma_f32_16x16x128_f8f6f4 v[204:207], v[122:127], v[38:43], 0 cbsz:2 blgp:2
	v_mfma_f32_16x16x128_f8f6f4 v[208:211], v[122:127], v[50:55], 0 cbsz:2 blgp:2
	v_mfma_f32_16x16x128_f8f6f4 v[212:215], v[122:127], v[62:67], v[188:191] cbsz:2 blgp:2
	s_waitcnt lgkmcnt(0)
	v_mfma_f32_16x16x128_f8f6f4 v[134:137], v[128:133], v[8:13], v[134:137] cbsz:2 blgp:2
	v_mfma_f32_16x16x128_f8f6f4 v[204:207], v[128:133], v[44:49], v[204:207] cbsz:2 blgp:2
	v_mfma_f32_16x16x128_f8f6f4 v[138:141], v[128:133], v[20:25], v[138:141] cbsz:2 blgp:2
	v_mfma_f32_16x16x128_f8f6f4 v[208:211], v[128:133], v[56:61], v[208:211] cbsz:2 blgp:2
	v_mfma_f32_16x16x128_f8f6f4 v[142:145], v[128:133], v[32:37], v[142:145] cbsz:2 blgp:2
	v_mfma_f32_16x16x128_f8f6f4 v[212:215], v[128:133], v[68:73], v[212:215] cbsz:2 blgp:2
	v_cndmask_b32_e64 v158, v134, v204, s[4:5]
	v_fma_mix_f32 v158, v158, v1, v147 op_sel_hi:[0,0,1]
	v_exp_f32_e32 v158, v158
	v_cndmask_b32_e64 v159, v138, v208, s[4:5]
	v_fma_mix_f32 v159, v159, v99, v151 op_sel_hi:[0,0,1]
	v_exp_f32_e32 v159, v159
	v_fma_f32 v158, v158, v186, v186
	v_rcp_f32_e32 v158, v158
	v_add_f32_e32 v159, 1.0, v159
	v_rcp_f32_e32 v159, v159
	v_cndmask_b32_e64 v160, v142, v212, s[4:5]
	v_fma_mix_f32 v161, v158, v160, v155 op_sel_hi:[0,0,1]
	v_exp_f32_e32 v161, v161
	s_add_u32 s48, s48, s40
	v_add_f32_e32 v161, 1.0, v161
	v_rcp_f32_e32 v161, v161
	s_addc_u32 s49, s49, s41
	v_fma_f32 v162, v161, -2.0, 1.0
	v_sub_f32_e32 v163, v176, v162
	v_fma_f32 v176, v159, v163, v162
	v_fma_f32 v164, |v176|, s16, v117
	v_fma_f32 v165, |v176|, s17, v118
	v_fma_f32 v166, |v176|, s18, v119
	v_lshrrev_b32_e32 v167, 26, v176
	v_min3_u32 v164, v164, v165, v166
	v_bfi_b32 v168, 31, v164, v167
	s_nop 1
	v_mul_u32_u24_dpp v170, v168, v180 quad_perm:[1,2,3,3] row_mask:0xf bank_mask:0xf bound_ctrl:1
	v_mad_u32_u24 v171, v168, v181, v170
	ds_write_b8_d16_hi v184, v171 offset:416
	global_store_short_d16_hi v185, v176, s[48:49]
	s_waitcnt lgkmcnt(0)
	s_barrier
	ds_read_b64 v[122:123], v106 offset:416
	ds_read_b64 v[124:125], v106 offset:424
	ds_read_b64 v[126:127], v106 offset:432
	s_barrier
	ds_read_b64 v[128:129], v106 offset:512
	ds_read_b64 v[130:131], v106 offset:520
	ds_read_b64 v[132:133], v106 offset:528
	s_waitcnt lgkmcnt(3)
	v_mfma_f32_16x16x128_f8f6f4 v[134:137], v[122:127], v[2:7], 0 cbsz:2 blgp:2
	v_mfma_f32_16x16x128_f8f6f4 v[138:141], v[122:127], v[14:19], 0 cbsz:2 blgp:2
	v_mfma_f32_16x16x128_f8f6f4 v[142:145], v[122:127], v[26:31], v[188:191] cbsz:2 blgp:2
	v_mfma_f32_16x16x128_f8f6f4 v[204:207], v[122:127], v[38:43], 0 cbsz:2 blgp:2
	v_mfma_f32_16x16x128_f8f6f4 v[208:211], v[122:127], v[50:55], 0 cbsz:2 blgp:2
	v_mfma_f32_16x16x128_f8f6f4 v[212:215], v[122:127], v[62:67], v[188:191] cbsz:2 blgp:2
	s_waitcnt lgkmcnt(0)
	v_mfma_f32_16x16x128_f8f6f4 v[134:137], v[128:133], v[8:13], v[134:137] cbsz:2 blgp:2
	v_mfma_f32_16x16x128_f8f6f4 v[204:207], v[128:133], v[44:49], v[204:207] cbsz:2 blgp:2
	v_mfma_f32_16x16x128_f8f6f4 v[138:141], v[128:133], v[20:25], v[138:141] cbsz:2 blgp:2
	v_mfma_f32_16x16x128_f8f6f4 v[208:211], v[128:133], v[56:61], v[208:211] cbsz:2 blgp:2
	v_mfma_f32_16x16x128_f8f6f4 v[142:145], v[128:133], v[32:37], v[142:145] cbsz:2 blgp:2
	v_mfma_f32_16x16x128_f8f6f4 v[212:215], v[128:133], v[68:73], v[212:215] cbsz:2 blgp:2
	v_cndmask_b32_e64 v158, v134, v204, s[4:5]
	v_fma_mix_f32 v158, v158, v1, v147 op_sel:[0,0,1] op_sel_hi:[0,0,1]
	v_exp_f32_e32 v158, v158
	v_cndmask_b32_e64 v159, v138, v208, s[4:5]
	v_fma_mix_f32 v159, v159, v99, v151 op_sel:[0,0,1] op_sel_hi:[0,0,1]
	v_exp_f32_e32 v159, v159
	v_fma_f32 v158, v158, v186, v186
	v_rcp_f32_e32 v158, v158
	v_add_f32_e32 v159, 1.0, v159
	v_rcp_f32_e32 v159, v159
	v_cndmask_b32_e64 v160, v142, v212, s[4:5]
	v_fma_mix_f32 v161, v158, v160, v155 op_sel:[0,0,1] op_sel_hi:[0,0,1]
	v_exp_f32_e32 v161, v161
	s_add_u32 s48, s48, s40
	v_add_f32_e32 v161, 1.0, v161
	v_rcp_f32_e32 v161, v161
	s_addc_u32 s49, s49, s41
	v_fma_f32 v162, v161, -2.0, 1.0
	v_sub_f32_e32 v163, v176, v162
	v_fma_f32 v176, v159, v163, v162
	v_fma_f32 v164, |v176|, s16, v117
	v_fma_f32 v165, |v176|, s17, v118
	v_fma_f32 v166, |v176|, s18, v119
	v_lshrrev_b32_e32 v167, 26, v176
	v_min3_u32 v164, v164, v165, v166
	v_bfi_b32 v168, 31, v164, v167
	s_nop 1
	v_mul_u32_u24_dpp v170, v168, v180 quad_perm:[1,2,3,3] row_mask:0xf bank_mask:0xf bound_ctrl:1
	v_mad_u32_u24 v171, v168, v181, v170
	ds_write_b8_d16_hi v184, v171
	global_store_short_d16_hi v185, v176, s[48:49]
	s_waitcnt lgkmcnt(0)
	s_barrier
	ds_read_b64 v[122:123], v106 offset:0
	ds_read_b64 v[124:125], v106 offset:8
	ds_read_b64 v[126:127], v106 offset:16
	s_barrier
	ds_read_b64 v[128:129], v106 offset:96
	ds_read_b64 v[130:131], v106 offset:104
	ds_read_b64 v[132:133], v106 offset:112
	s_waitcnt lgkmcnt(3)
	v_mfma_f32_16x16x128_f8f6f4 v[134:137], v[122:127], v[2:7], 0 cbsz:2 blgp:2
	v_mfma_f32_16x16x128_f8f6f4 v[138:141], v[122:127], v[14:19], 0 cbsz:2 blgp:2
	v_mfma_f32_16x16x128_f8f6f4 v[142:145], v[122:127], v[26:31], v[188:191] cbsz:2 blgp:2
	v_mfma_f32_16x16x128_f8f6f4 v[204:207], v[122:127], v[38:43], 0 cbsz:2 blgp:2
	v_mfma_f32_16x16x128_f8f6f4 v[208:211], v[122:127], v[50:55], 0 cbsz:2 blgp:2
	v_mfma_f32_16x16x128_f8f6f4 v[212:215], v[122:127], v[62:67], v[188:191] cbsz:2 blgp:2
	s_waitcnt lgkmcnt(0)
	v_mfma_f32_16x16x128_f8f6f4 v[134:137], v[128:133], v[8:13], v[134:137] cbsz:2 blgp:2
	v_mfma_f32_16x16x128_f8f6f4 v[204:207], v[128:133], v[44:49], v[204:207] cbsz:2 blgp:2
	v_mfma_f32_16x16x128_f8f6f4 v[138:141], v[128:133], v[20:25], v[138:141] cbsz:2 blgp:2
	v_mfma_f32_16x16x128_f8f6f4 v[208:211], v[128:133], v[56:61], v[208:211] cbsz:2 blgp:2
	v_mfma_f32_16x16x128_f8f6f4 v[142:145], v[128:133], v[32:37], v[142:145] cbsz:2 blgp:2
	v_mfma_f32_16x16x128_f8f6f4 v[212:215], v[128:133], v[68:73], v[212:215] cbsz:2 blgp:2
	v_cndmask_b32_e64 v158, v134, v204, s[4:5]
	v_fma_mix_f32 v158, v158, v1, v148 op_sel_hi:[0,0,1]
	v_exp_f32_e32 v158, v158
	v_cndmask_b32_e64 v159, v138, v208, s[4:5]
	v_fma_mix_f32 v159, v159, v99, v152 op_sel_hi:[0,0,1]
	v_exp_f32_e32 v159, v159
	v_fma_f32 v158, v158, v186, v186
	v_rcp_f32_e32 v158, v158
	v_add_f32_e32 v159, 1.0, v159
	v_rcp_f32_e32 v159, v159
	v_cndmask_b32_e64 v160, v142, v212, s[4:5]
	v_fma_mix_f32 v161, v158, v160, v156 op_sel_hi:[0,0,1]
	v_exp_f32_e32 v161, v161
	s_add_u32 s48, s48, s40
	v_add_f32_e32 v161, 1.0, v161
	v_rcp_f32_e32 v161, v161
	s_addc_u32 s49, s49, s41
	v_fma_f32 v162, v161, -2.0, 1.0
	v_sub_f32_e32 v163, v176, v162
	v_fma_f32 v176, v159, v163, v162
	v_fma_f32 v164, |v176|, s16, v117
	v_fma_f32 v165, |v176|, s17, v118
	v_fma_f32 v166, |v176|, s18, v119
	v_lshrrev_b32_e32 v167, 26, v176
	v_min3_u32 v164, v164, v165, v166
	v_bfi_b32 v168, 31, v164, v167
	s_nop 1
	v_mul_u32_u24_dpp v170, v168, v180 quad_perm:[1,2,3,3] row_mask:0xf bank_mask:0xf bound_ctrl:1
	v_mad_u32_u24 v171, v168, v181, v170
	ds_write_b8_d16_hi v184, v171 offset:416
	global_store_short_d16_hi v185, v176, s[48:49]
	s_waitcnt lgkmcnt(0)
	s_barrier
	ds_read_b64 v[122:123], v106 offset:416
	ds_read_b64 v[124:125], v106 offset:424
	ds_read_b64 v[126:127], v106 offset:432
	s_barrier
	ds_read_b64 v[128:129], v106 offset:512
	ds_read_b64 v[130:131], v106 offset:520
	ds_read_b64 v[132:133], v106 offset:528
	s_waitcnt lgkmcnt(3)
	v_mfma_f32_16x16x128_f8f6f4 v[134:137], v[122:127], v[2:7], 0 cbsz:2 blgp:2
	v_mfma_f32_16x16x128_f8f6f4 v[138:141], v[122:127], v[14:19], 0 cbsz:2 blgp:2
	v_mfma_f32_16x16x128_f8f6f4 v[142:145], v[122:127], v[26:31], v[188:191] cbsz:2 blgp:2
	v_mfma_f32_16x16x128_f8f6f4 v[204:207], v[122:127], v[38:43], 0 cbsz:2 blgp:2
	v_mfma_f32_16x16x128_f8f6f4 v[208:211], v[122:127], v[50:55], 0 cbsz:2 blgp:2
	v_mfma_f32_16x16x128_f8f6f4 v[212:215], v[122:127], v[62:67], v[188:191] cbsz:2 blgp:2
	s_waitcnt lgkmcnt(0)
	v_mfma_f32_16x16x128_f8f6f4 v[134:137], v[128:133], v[8:13], v[134:137] cbsz:2 blgp:2
	v_mfma_f32_16x16x128_f8f6f4 v[204:207], v[128:133], v[44:49], v[204:207] cbsz:2 blgp:2
	v_mfma_f32_16x16x128_f8f6f4 v[138:141], v[128:133], v[20:25], v[138:141] cbsz:2 blgp:2
	v_mfma_f32_16x16x128_f8f6f4 v[208:211], v[128:133], v[56:61], v[208:211] cbsz:2 blgp:2
	v_mfma_f32_16x16x128_f8f6f4 v[142:145], v[128:133], v[32:37], v[142:145] cbsz:2 blgp:2
	v_mfma_f32_16x16x128_f8f6f4 v[212:215], v[128:133], v[68:73], v[212:215] cbsz:2 blgp:2
	v_cndmask_b32_e64 v158, v134, v204, s[4:5]
	v_fma_mix_f32 v158, v158, v1, v148 op_sel:[0,0,1] op_sel_hi:[0,0,1]
	v_exp_f32_e32 v158, v158
	v_cndmask_b32_e64 v159, v138, v208, s[4:5]
	v_fma_mix_f32 v159, v159, v99, v152 op_sel:[0,0,1] op_sel_hi:[0,0,1]
	v_exp_f32_e32 v159, v159
	v_fma_f32 v158, v158, v186, v186
	v_rcp_f32_e32 v158, v158
	v_add_f32_e32 v159, 1.0, v159
	v_rcp_f32_e32 v159, v159
	v_cndmask_b32_e64 v160, v142, v212, s[4:5]
	v_fma_mix_f32 v161, v158, v160, v156 op_sel:[0,0,1] op_sel_hi:[0,0,1]
	v_exp_f32_e32 v161, v161
	s_add_u32 s48, s48, s40
	v_add_f32_e32 v161, 1.0, v161
	v_rcp_f32_e32 v161, v161
	s_addc_u32 s49, s49, s41
	v_fma_f32 v162, v161, -2.0, 1.0
	v_sub_f32_e32 v163, v176, v162
	v_fma_f32 v176, v159, v163, v162
	v_fma_f32 v164, |v176|, s16, v117
	v_fma_f32 v165, |v176|, s17, v118
	v_fma_f32 v166, |v176|, s18, v119
	v_lshrrev_b32_e32 v167, 26, v176
	v_min3_u32 v164, v164, v165, v166
	v_bfi_b32 v168, 31, v164, v167
	s_nop 1
	v_mul_u32_u24_dpp v170, v168, v180 quad_perm:[1,2,3,3] row_mask:0xf bank_mask:0xf bound_ctrl:1
	v_mad_u32_u24 v171, v168, v181, v170
	ds_write_b8_d16_hi v184, v171
	global_store_short_d16_hi v185, v176, s[48:49]
	s_waitcnt lgkmcnt(0)
	s_barrier
	ds_read_b64 v[122:123], v106 offset:0
	ds_read_b64 v[124:125], v106 offset:8
	ds_read_b64 v[126:127], v106 offset:16
	s_barrier
	ds_read_b64 v[128:129], v106 offset:96
	ds_read_b64 v[130:131], v106 offset:104
	ds_read_b64 v[132:133], v106 offset:112
	s_waitcnt lgkmcnt(3)
	v_mfma_f32_16x16x128_f8f6f4 v[134:137], v[122:127], v[2:7], 0 cbsz:2 blgp:2
	v_mfma_f32_16x16x128_f8f6f4 v[138:141], v[122:127], v[14:19], 0 cbsz:2 blgp:2
	v_mfma_f32_16x16x128_f8f6f4 v[142:145], v[122:127], v[26:31], v[188:191] cbsz:2 blgp:2
	v_mfma_f32_16x16x128_f8f6f4 v[204:207], v[122:127], v[38:43], 0 cbsz:2 blgp:2
	v_mfma_f32_16x16x128_f8f6f4 v[208:211], v[122:127], v[50:55], 0 cbsz:2 blgp:2
	v_mfma_f32_16x16x128_f8f6f4 v[212:215], v[122:127], v[62:67], v[188:191] cbsz:2 blgp:2
	s_waitcnt lgkmcnt(0)
	v_mfma_f32_16x16x128_f8f6f4 v[134:137], v[128:133], v[8:13], v[134:137] cbsz:2 blgp:2
	v_mfma_f32_16x16x128_f8f6f4 v[204:207], v[128:133], v[44:49], v[204:207] cbsz:2 blgp:2
	v_mfma_f32_16x16x128_f8f6f4 v[138:141], v[128:133], v[20:25], v[138:141] cbsz:2 blgp:2
	v_mfma_f32_16x16x128_f8f6f4 v[208:211], v[128:133], v[56:61], v[208:211] cbsz:2 blgp:2
	v_mfma_f32_16x16x128_f8f6f4 v[142:145], v[128:133], v[32:37], v[142:145] cbsz:2 blgp:2
	v_mfma_f32_16x16x128_f8f6f4 v[212:215], v[128:133], v[68:73], v[212:215] cbsz:2 blgp:2
	v_cndmask_b32_e64 v158, v134, v204, s[4:5]
	v_fma_mix_f32 v158, v158, v1, v149 op_sel_hi:[0,0,1]
	v_exp_f32_e32 v158, v158
	v_cndmask_b32_e64 v159, v138, v208, s[4:5]
	v_fma_mix_f32 v159, v159, v99, v153 op_sel_hi:[0,0,1]
	v_exp_f32_e32 v159, v159
	v_fma_f32 v158, v158, v186, v186
	v_rcp_f32_e32 v158, v158
	v_add_f32_e32 v159, 1.0, v159
	v_rcp_f32_e32 v159, v159
	v_cndmask_b32_e64 v160, v142, v212, s[4:5]
	v_fma_mix_f32 v161, v158, v160, v157 op_sel_hi:[0,0,1]
	v_exp_f32_e32 v161, v161
	s_add_u32 s48, s48, s40
	v_add_f32_e32 v161, 1.0, v161
	v_rcp_f32_e32 v161, v161
	s_addc_u32 s49, s49, s41
	v_fma_f32 v162, v161, -2.0, 1.0
	v_sub_f32_e32 v163, v176, v162
	v_fma_f32 v176, v159, v163, v162
	v_fma_f32 v164, |v176|, s16, v117
	v_fma_f32 v165, |v176|, s17, v118
	v_fma_f32 v166, |v176|, s18, v119
	v_lshrrev_b32_e32 v167, 26, v176
	v_min3_u32 v164, v164, v165, v166
	v_bfi_b32 v168, 31, v164, v167
	s_nop 1
	v_mul_u32_u24_dpp v170, v168, v180 quad_perm:[1,2,3,3] row_mask:0xf bank_mask:0xf bound_ctrl:1
	v_mad_u32_u24 v171, v168, v181, v170
	ds_write_b8_d16_hi v184, v171 offset:416
	global_store_short_d16_hi v185, v176, s[48:49]
	s_waitcnt lgkmcnt(0)
	s_barrier
	ds_read_b64 v[122:123], v106 offset:416
	ds_read_b64 v[124:125], v106 offset:424
	ds_read_b64 v[126:127], v106 offset:432
	s_barrier
	ds_read_b64 v[128:129], v106 offset:512
	ds_read_b64 v[130:131], v106 offset:520
	ds_read_b64 v[132:133], v106 offset:528
	s_add_i32 s44, s44, 16
	s_waitcnt lgkmcnt(3)
	v_mfma_f32_16x16x128_f8f6f4 v[134:137], v[122:127], v[2:7], 0 cbsz:2 blgp:2
	v_mfma_f32_16x16x128_f8f6f4 v[138:141], v[122:127], v[14:19], 0 cbsz:2 blgp:2
	v_mfma_f32_16x16x128_f8f6f4 v[142:145], v[122:127], v[26:31], v[188:191] cbsz:2 blgp:2
	v_mfma_f32_16x16x128_f8f6f4 v[204:207], v[122:127], v[38:43], 0 cbsz:2 blgp:2
	v_mfma_f32_16x16x128_f8f6f4 v[208:211], v[122:127], v[50:55], 0 cbsz:2 blgp:2
	v_mfma_f32_16x16x128_f8f6f4 v[212:215], v[122:127], v[62:67], v[188:191] cbsz:2 blgp:2
	s_waitcnt lgkmcnt(0)
	v_mfma_f32_16x16x128_f8f6f4 v[134:137], v[128:133], v[8:13], v[134:137] cbsz:2 blgp:2
	v_mfma_f32_16x16x128_f8f6f4 v[204:207], v[128:133], v[44:49], v[204:207] cbsz:2 blgp:2
	v_mfma_f32_16x16x128_f8f6f4 v[138:141], v[128:133], v[20:25], v[138:141] cbsz:2 blgp:2
	v_mfma_f32_16x16x128_f8f6f4 v[208:211], v[128:133], v[56:61], v[208:211] cbsz:2 blgp:2
	v_mfma_f32_16x16x128_f8f6f4 v[142:145], v[128:133], v[32:37], v[142:145] cbsz:2 blgp:2
	v_mfma_f32_16x16x128_f8f6f4 v[212:215], v[128:133], v[68:73], v[212:215] cbsz:2 blgp:2
	v_cndmask_b32_e64 v158, v134, v204, s[4:5]
	v_fma_mix_f32 v158, v158, v1, v149 op_sel:[0,0,1] op_sel_hi:[0,0,1]
	v_exp_f32_e32 v158, v158
	v_cndmask_b32_e64 v159, v138, v208, s[4:5]
	v_fma_mix_f32 v159, v159, v99, v153 op_sel:[0,0,1] op_sel_hi:[0,0,1]
	v_exp_f32_e32 v159, v159
	v_fma_f32 v158, v158, v186, v186
	v_rcp_f32_e32 v158, v158
	v_add_f32_e32 v159, 1.0, v159
	v_rcp_f32_e32 v159, v159
	v_cndmask_b32_e64 v160, v142, v212, s[4:5]
	v_fma_mix_f32 v161, v158, v160, v157 op_sel:[0,0,1] op_sel_hi:[0,0,1]
	v_exp_f32_e32 v161, v161
	s_add_u32 s48, s48, s40
	v_add_f32_e32 v161, 1.0, v161
	v_rcp_f32_e32 v161, v161
	s_addc_u32 s49, s49, s41
	v_fma_f32 v162, v161, -2.0, 1.0
	v_sub_f32_e32 v163, v176, v162
	v_fma_f32 v176, v159, v163, v162
	v_fma_f32 v164, |v176|, s16, v117
	v_fma_f32 v165, |v176|, s17, v118
	v_fma_f32 v166, |v176|, s18, v119
	v_lshrrev_b32_e32 v167, 26, v176
	v_min3_u32 v164, v164, v165, v166
	v_bfi_b32 v168, 31, v164, v167
	s_nop 1
	v_mul_u32_u24_dpp v170, v168, v180 quad_perm:[1,2,3,3] row_mask:0xf bank_mask:0xf bound_ctrl:1
	v_mad_u32_u24 v171, v168, v181, v170
	ds_write_b8_d16_hi v184, v171
	global_store_short_d16_hi v185, v176, s[48:49]
	s_waitcnt lgkmcnt(0)
	s_barrier
	ds_read_b64 v[122:123], v106 offset:0
	ds_read_b64 v[124:125], v106 offset:8
	ds_read_b64 v[126:127], v106 offset:16
	s_cmp_lt_i32 s44, s45
	s_barrier
	s_cbranch_scc1 .Lscan_loop_a_st
	s_branch .Lscan_exit_st
	.p2align 6

.LBB2_12:
	s_or_b64 exec, exec, s[0:1]
	v_and_b32_e32 v97, 1, v74
	v_mov_b32_e32 v74, s8
	v_mov_b32_e32 v75, s9
	v_lshl_or_b32 v76, s2, 9, v0
	v_mov_b32_e32 v77, v87
	v_lshl_add_u64 v[74:75], v[76:77], 2, v[74:75]
	s_waitcnt lgkmcnt(0)
	s_barrier
	global_load_dword v118, v[74:75], off
	v_and_b32_e32 v74, 4, v90
	v_mov_b32_e32 v75, 0xd0
	v_cmp_ne_u32_e32 vcc, 0, v74
	v_and_b32_e32 v110, 3, v0
	v_cmp_gt_u32_e64 s[0:1], 12, v90
	v_cndmask_b32_e32 v74, 0, v75, vcc
	v_cmp_eq_u32_e32 vcc, 0, v110
	s_and_b64 s[4:5], vcc, s[0:1]
	s_lshl_b32 s1, s2, 21
	v_add_u32_e32 v109, v74, v86
	s_mul_i32 s0, s2, 0x600000
	v_lshl_or_b32 v74, v89, 1, v88
	s_and_b32 s2, s1, 0x1e00000
	v_mul_u32_u24_e32 v74, 0x60, v74
	v_lshlrev_b32_e32 v75, 1, v90
	s_add_u32 s0, s14, s0
	s_addc_u32 s1, s15, 0
	v_or3_b32 v86, v74, v75, v97
	v_lshl_add_u64 v[98:99], v[86:87], 4, s[0:1]
	s_mov_b64 s[0:1], 0x5a0000
	v_lshl_add_u64 v[100:101], v[98:99], 0, s[0:1]
	s_mov_b32 s0, 0x5a0000
	v_add_co_u32_e32 v102, vcc, s0, v98
	s_waitcnt vmcnt(4)
	v_mul_f32_e32 v86, 0xbfb8aa3b, v95
	v_addc_co_u32_e32 v103, vcc, 0, v99, vcc
	global_load_dwordx4 v[82:85], v[102:103], off
	global_load_dwordx4 v[74:77], v[100:101], off offset:512
	global_load_dwordx4 v[78:81], v[100:101], off offset:1024
	v_mul_f32_e32 v100, 0x3c91a2b4, v86
	s_waitcnt vmcnt(6)
	v_mul_f32_e32 v86, 0xbfb8aa3b, v94
	v_mul_f32_e32 v101, 0x3c91a2b4, v86
	s_waitcnt vmcnt(5)
	v_mul_f32_e32 v86, 0x4038aa3b, v93
	v_and_b32_e32 v0, 12, v0
	v_mul_f32_e32 v102, 0x3c91a2b4, v86
	v_lshrrev_b32_e32 v86, 2, v90
	v_mul_u32_u24_e32 v90, 0xd0, v97
	v_mad_u32_u24 v0, v89, 24, v0
	v_mul_u32_u24_e32 v88, 12, v88
	v_add3_u32 v93, v0, v90, v88
	v_or_b32_e32 v0, s2, v1
	v_lshlrev_b32_e32 v104, 3, v86
	v_lshlrev_b32_e32 v89, 20, v97
	v_lshl_add_u32 v0, s22, 8, v0
	v_sub_u32_e32 v86, 0, v104
	v_or3_b32 v0, v0, v89, v92
	v_and_b32_e32 v111, 24, v86
	v_lshlrev_b32_e32 v86, 1, v0
	s_mov_b64 s[6:7], 0x5a6000
	v_lshl_add_u64 v[0:1], s[12:13], 0, v[86:87]
	v_lshl_add_u64 v[86:87], v[98:99], 0, s[6:7]
	s_mov_b64 s[6:7], 0x5a6200
	v_lshl_add_u64 v[88:89], v[98:99], 0, s[6:7]
	s_mov_b64 s[6:7], 0x5a6400
	v_cmp_lt_u32_e64 s[0:1], 1, v91
	s_waitcnt vmcnt(4)
	v_mul_f32_e32 v103, 0x4038aa3b, v96
	s_mov_b32 s3, 0
	v_or_b32_e32 v105, 0x1c400, v109
	v_add_u32_e32 v106, 0x1c410, v109
	v_add_u32_e32 v107, 0x1c470, v109
	v_add_u32_e32 v108, 0x1c5b0, v109
	v_add_u32_e32 v109, 0x1c610, v109
	v_mul_u32_u24_e32 v110, 6, v110
	v_lshl_add_u64 v[90:91], v[98:99], 0, s[6:7]
	s_movk_i32 s22, 0x780
	s_movk_i32 s14, 0x7f
	s_movk_i32 s15, 0xf0
	v_mov_b32_e32 v112, 0x7f7f7f7f
	s_mov_b32 s17, 0x42700000
	s_mov_b32 s18, 0x41f00000
	s_mov_b32 s19, 0x41700000
	s_mov_b64 s[6:7], 0x12000
	s_mov_b64 s[8:9], 0x12200
	s_mov_b64 s[10:11], 0x12400
	v_mov_b32_e32 v113, 0x4b400000
	v_mov_b32_e32 v114, 0x4b400008
	v_mov_b32_e32 v115, 0x4b400010
	v_add_u32_e32 v116, 0x1c5a0, v93
	v_add_u32_e32 v117, 0x1c400, v93
	v_mbcnt_lo_u32_b32 v200, -1, 0
	v_mbcnt_hi_u32_b32 v200, -1, v200
	v_and_b32_e32 v201, 3, v200
	v_and_b32_e32 v202, 15, v200
	v_cmp_gt_u32_e32 vcc, 8, v202
	s_nop 1
	v_cndmask_b32_e64 v178, 0, v112, vcc
	v_cndmask_b32_e64 v179, v112, 0, vcc
	v_lshlrev_b32_e32 v181, 1, v201
	v_sub_u32_e32 v202, 22, v181
	v_lshlrev_b32_e64 v180, v202, 1
	v_sub_u32_e32 v202, 16, v181
	v_lshlrev_b32_e64 v181, v202, 1
	v_lshrrev_b32_e32 v202, 3, v104
	v_sub_u32_e32 v184, v117, v202
	v_add_u32_e32 v184, v184, v201
	v_add_u32_e32 v202, 0x1c4c0, v202
	v_cmp_eq_u32_e32 vcc, 3, v201
	s_nop 1
	v_cndmask_b32_e32 v184, v184, v202, vcc
	v_subrev_u32_e32 v185, s12, v0
	s_movk_i32 s44, 0x780
	s_movk_i32 s45, 0x800
	s_lshr_b32 s46, s44, 3
	s_add_i32 s46, s46, 1
	s_mul_i32 s46, s46, 0x6000
	s_mov_b32 s47, 0
	v_lshl_add_u64 v[196:197], v[98:99], 0, s[46:47]
	s_mov_b32 s42, 0x6000
	s_mov_b32 s43, 0
	s_sub_i32 s46, s44, 1
	s_sub_i32 s47, 0x800, s44
	s_and_b64 s[40:41], s[20:21], exec
	s_cselect_b32 s46, s46, s47
	s_cselect_b32 s41, 0, -1
	s_xor_b32 s40, s41, 0x400
	s_sub_i32 s40, s40, s41
	s_ashr_i32 s47, s46, 31
	s_lshl_b64 s[46:47], s[46:47], 10
	s_add_u32 s48, s12, s46
	s_addc_u32 s49, s13, s47
	v_readfirstlane_b32 s51, v117
	s_waitcnt vmcnt(0) lgkmcnt(0)
	v_mov_b32_e32 v176, v118
	v_rcp_f32_e32 v186, v102
	s_nop 1
	v_mul_f32_e32 v188, v103, v186
	v_mov_b32_e32 v189, 0
	v_mov_b32_e32 v190, 0
	v_mov_b32_e32 v191, 0
	s_nop 1
	s_sub_u32 s51, s51, 0x1c400
	s_cmp_lt_i32 s44, s45
	s_cbranch_scc0 .Lscan_exit_f2
	ds_read_b64 v[122:123], v105 offset:0
	ds_read_b64 v[124:125], v105 offset:8
	ds_read_b64 v[126:127], v105 offset:16
	s_waitcnt lgkmcnt(0)
	s_cmp_lt_u32 s51, 96
	s_cbranch_scc0 .Lscan_loop_b_f2
	.p2align 6
.Lscan_loop_a_f2:
	ds_read_b64 v[128:129], v105 offset:96
	ds_read_b64 v[130:131], v105 offset:104
	ds_read_b64 v[132:133], v105 offset:112
	s_waitcnt vmcnt(8)
	global_load_dwordx4 v[146:149], v[196:197], off
	global_load_dwordx4 v[150:153], v[196:197], off offset:512
	global_load_dwordx4 v[154:157], v[196:197], off offset:1024
	v_lshl_add_u64 v[196:197], v[196:197], 0, s[42:43]
	s_waitcnt lgkmcnt(3)
	v_mfma_f32_16x16x128_f8f6f4 v[134:137], v[122:127], v[2:7], 0 cbsz:2 blgp:2
	v_mfma_f32_16x16x128_f8f6f4 v[138:141], v[122:127], v[14:19], 0 cbsz:2 blgp:2
	v_mfma_f32_16x16x128_f8f6f4 v[142:145], v[122:127], v[26:31], v[188:191] cbsz:2 blgp:2
	v_mfma_f32_16x16x128_f8f6f4 v[204:207], v[122:127], v[38:43], 0 cbsz:2 blgp:2
	v_mfma_f32_16x16x128_f8f6f4 v[208:211], v[122:127], v[50:55], 0 cbsz:2 blgp:2
	v_mfma_f32_16x16x128_f8f6f4 v[212:215], v[122:127], v[62:67], v[188:191] cbsz:2 blgp:2
	s_waitcnt lgkmcnt(0)
	v_mfma_f32_16x16x128_f8f6f4 v[134:137], v[128:133], v[8:13], v[134:137] cbsz:2 blgp:2
	v_mfma_f32_16x16x128_f8f6f4 v[204:207], v[128:133], v[44:49], v[204:207] cbsz:2 blgp:2
	v_mfma_f32_16x16x128_f8f6f4 v[138:141], v[128:133], v[20:25], v[138:141] cbsz:2 blgp:2
	v_mfma_f32_16x16x128_f8f6f4 v[208:211], v[128:133], v[56:61], v[208:211] cbsz:2 blgp:2
	v_mfma_f32_16x16x128_f8f6f4 v[142:145], v[128:133], v[32:37], v[142:145] cbsz:2 blgp:2
	v_mfma_f32_16x16x128_f8f6f4 v[212:215], v[128:133], v[68:73], v[212:215] cbsz:2 blgp:2
	v_cndmask_b32_e64 v158, v134, v204, s[0:1]
	v_fma_mix_f32 v158, v158, v100, v82 op_sel_hi:[0,0,1]
	v_exp_f32_e32 v158, v158
	v_cndmask_b32_e64 v159, v138, v208, s[0:1]
	v_fma_mix_f32 v159, v159, v101, v74 op_sel_hi:[0,0,1]
	v_exp_f32_e32 v159, v159
	v_fma_f32 v158, v158, v186, v186
	v_rcp_f32_e32 v158, v158
	v_add_f32_e32 v159, 1.0, v159
	v_rcp_f32_e32 v159, v159
	v_cndmask_b32_e64 v160, v142, v212, s[0:1]
	v_fma_mix_f32 v161, v158, v160, v78 op_sel_hi:[0,0,1]
	v_exp_f32_e32 v161, v161
	s_add_u32 s48, s48, s40
	v_add_f32_e32 v161, 1.0, v161
	v_rcp_f32_e32 v161, v161
	s_addc_u32 s49, s49, s41
	v_fma_f32 v162, v161, -2.0, 1.0
	v_sub_f32_e32 v163, v176, v162
	v_fma_f32 v176, v159, v163, v162
	v_fma_f32 v164, |v176|, s17, v113
	v_fma_f32 v165, |v176|, s18, v114
	v_fma_f32 v166, |v176|, s19, v115
	v_lshrrev_b32_e32 v167, 26, v176
	v_min3_u32 v164, v164, v165, v166
	v_bfi_b32 v168, 31, v164, v167
	s_nop 1
	v_mul_u32_u24_dpp v170, v168, v180 quad_perm:[1,2,3,3] row_mask:0xf bank_mask:0xf bound_ctrl:1
	v_mad_u32_u24 v171, v168, v181, v170
	ds_write_b8_d16_hi v184, v171 offset:416
	global_store_short_d16_hi v185, v176, s[48:49]
	s_waitcnt lgkmcnt(0)
	s_barrier
	ds_read_b64 v[122:123], v105 offset:416
	ds_read_b64 v[124:125], v105 offset:424
	ds_read_b64 v[126:127], v105 offset:432
	s_barrier
	ds_read_b64 v[128:129], v105 offset:512
	ds_read_b64 v[130:131], v105 offset:520
	ds_read_b64 v[132:133], v105 offset:528
	s_waitcnt lgkmcnt(3)
	v_mfma_f32_16x16x128_f8f6f4 v[134:137], v[122:127], v[2:7], 0 cbsz:2 blgp:2
	v_mfma_f32_16x16x128_f8f6f4 v[138:141], v[122:127], v[14:19], 0 cbsz:2 blgp:2
	v_mfma_f32_16x16x128_f8f6f4 v[142:145], v[122:127], v[26:31], v[188:191] cbsz:2 blgp:2
	v_mfma_f32_16x16x128_f8f6f4 v[204:207], v[122:127], v[38:43], 0 cbsz:2 blgp:2
	v_mfma_f32_16x16x128_f8f6f4 v[208:211], v[122:127], v[50:55], 0 cbsz:2 blgp:2
	v_mfma_f32_16x16x128_f8f6f4 v[212:215], v[122:127], v[62:67], v[188:191] cbsz:2 blgp:2
	s_waitcnt lgkmcnt(0)
	v_mfma_f32_16x16x128_f8f6f4 v[134:137], v[128:133], v[8:13], v[134:137] cbsz:2 blgp:2
	v_mfma_f32_16x16x128_f8f6f4 v[204:207], v[128:133], v[44:49], v[204:207] cbsz:2 blgp:2
	v_mfma_f32_16x16x128_f8f6f4 v[138:141], v[128:133], v[20:25], v[138:141] cbsz:2 blgp:2
	v_mfma_f32_16x16x128_f8f6f4 v[208:211], v[128:133], v[56:61], v[208:211] cbsz:2 blgp:2
	v_mfma_f32_16x16x128_f8f6f4 v[142:145], v[128:133], v[32:37], v[142:145] cbsz:2 blgp:2
	v_mfma_f32_16x16x128_f8f6f4 v[212:215], v[128:133], v[68:73], v[212:215] cbsz:2 blgp:2
	v_cndmask_b32_e64 v158, v134, v204, s[0:1]
	v_fma_mix_f32 v158, v158, v100, v82 op_sel:[0,0,1] op_sel_hi:[0,0,1]
	v_exp_f32_e32 v158, v158
	v_cndmask_b32_e64 v159, v138, v208, s[0:1]
	v_fma_mix_f32 v159, v159, v101, v74 op_sel:[0,0,1] op_sel_hi:[0,0,1]
	v_exp_f32_e32 v159, v159
	v_fma_f32 v158, v158, v186, v186
	v_rcp_f32_e32 v158, v158
	v_add_f32_e32 v159, 1.0, v159
	v_rcp_f32_e32 v159, v159
	v_cndmask_b32_e64 v160, v142, v212, s[0:1]
	v_fma_mix_f32 v161, v158, v160, v78 op_sel:[0,0,1] op_sel_hi:[0,0,1]
	v_exp_f32_e32 v161, v161
	s_add_u32 s48, s48, s40
	v_add_f32_e32 v161, 1.0, v161
	v_rcp_f32_e32 v161, v161
	s_addc_u32 s49, s49, s41
	v_fma_f32 v162, v161, -2.0, 1.0
	v_sub_f32_e32 v163, v176, v162
	v_fma_f32 v176, v159, v163, v162
	v_fma_f32 v164, |v176|, s17, v113
	v_fma_f32 v165, |v176|, s18, v114
	v_fma_f32 v166, |v176|, s19, v115
	v_lshrrev_b32_e32 v167, 26, v176
	v_min3_u32 v164, v164, v165, v166
	v_bfi_b32 v168, 31, v164, v167
	s_nop 1
	v_mul_u32_u24_dpp v170, v168, v180 quad_perm:[1,2,3,3] row_mask:0xf bank_mask:0xf bound_ctrl:1
	v_mad_u32_u24 v171, v168, v181, v170
	ds_write_b8_d16_hi v184, v171
	global_store_short_d16_hi v185, v176, s[48:49]
	s_waitcnt lgkmcnt(0)
	s_barrier
	ds_read_b64 v[122:123], v105 offset:0
	ds_read_b64 v[124:125], v105 offset:8
	ds_read_b64 v[126:127], v105 offset:16
	s_barrier
	ds_read_b64 v[128:129], v105 offset:96
	ds_read_b64 v[130:131], v105 offset:104
	ds_read_b64 v[132:133], v105 offset:112
	s_waitcnt lgkmcnt(3)
	v_mfma_f32_16x16x128_f8f6f4 v[134:137], v[122:127], v[2:7], 0 cbsz:2 blgp:2
	v_mfma_f32_16x16x128_f8f6f4 v[138:141], v[122:127], v[14:19], 0 cbsz:2 blgp:2
	v_mfma_f32_16x16x128_f8f6f4 v[142:145], v[122:127], v[26:31], v[188:191] cbsz:2 blgp:2
	v_mfma_f32_16x16x128_f8f6f4 v[204:207], v[122:127], v[38:43], 0 cbsz:2 blgp:2
	v_mfma_f32_16x16x128_f8f6f4 v[208:211], v[122:127], v[50:55], 0 cbsz:2 blgp:2
	v_mfma_f32_16x16x128_f8f6f4 v[212:215], v[122:127], v[62:67], v[188:191] cbsz:2 blgp:2
	s_waitcnt lgkmcnt(0)
	v_mfma_f32_16x16x128_f8f6f4 v[134:137], v[128:133], v[8:13], v[134:137] cbsz:2 blgp:2
	v_mfma_f32_16x16x128_f8f6f4 v[204:207], v[128:133], v[44:49], v[204:207] cbsz:2 blgp:2
	v_mfma_f32_16x16x128_f8f6f4 v[138:141], v[128:133], v[20:25], v[138:141] cbsz:2 blgp:2
	v_mfma_f32_16x16x128_f8f6f4 v[208:211], v[128:133], v[56:61], v[208:211] cbsz:2 blgp:2
	v_mfma_f32_16x16x128_f8f6f4 v[142:145], v[128:133], v[32:37], v[142:145] cbsz:2 blgp:2
	v_mfma_f32_16x16x128_f8f6f4 v[212:215], v[128:133], v[68:73], v[212:215] cbsz:2 blgp:2
	v_cndmask_b32_e64 v158, v134, v204, s[0:1]
	v_fma_mix_f32 v158, v158, v100, v83 op_sel_hi:[0,0,1]
	v_exp_f32_e32 v158, v158
	v_cndmask_b32_e64 v159, v138, v208, s[0:1]
	v_fma_mix_f32 v159, v159, v101, v75 op_sel_hi:[0,0,1]
	v_exp_f32_e32 v159, v159
	v_fma_f32 v158, v158, v186, v186
	v_rcp_f32_e32 v158, v158
	v_add_f32_e32 v159, 1.0, v159
	v_rcp_f32_e32 v159, v159
	v_cndmask_b32_e64 v160, v142, v212, s[0:1]
	v_fma_mix_f32 v161, v158, v160, v79 op_sel_hi:[0,0,1]
	v_exp_f32_e32 v161, v161
	s_add_u32 s48, s48, s40
	v_add_f32_e32 v161, 1.0, v161
	v_rcp_f32_e32 v161, v161
	s_addc_u32 s49, s49, s41
	v_fma_f32 v162, v161, -2.0, 1.0
	v_sub_f32_e32 v163, v176, v162
	v_fma_f32 v176, v159, v163, v162
	v_fma_f32 v164, |v176|, s17, v113
	v_fma_f32 v165, |v176|, s18, v114
	v_fma_f32 v166, |v176|, s19, v115
	v_lshrrev_b32_e32 v167, 26, v176
	v_min3_u32 v164, v164, v165, v166
	v_bfi_b32 v168, 31, v164, v167
	s_nop 1
	v_mul_u32_u24_dpp v170, v168, v180 quad_perm:[1,2,3,3] row_mask:0xf bank_mask:0xf bound_ctrl:1
	v_mad_u32_u24 v171, v168, v181, v170
	ds_write_b8_d16_hi v184, v171 offset:416
	global_store_short_d16_hi v185, v176, s[48:49]
	s_waitcnt lgkmcnt(0)
	s_barrier
	ds_read_b64 v[122:123], v105 offset:416
	ds_read_b64 v[124:125], v105 offset:424
	ds_read_b64 v[126:127], v105 offset:432
	s_barrier
	ds_read_b64 v[128:129], v105 offset:512
	ds_read_b64 v[130:131], v105 offset:520
	ds_read_b64 v[132:133], v105 offset:528
	s_waitcnt lgkmcnt(3)
	v_mfma_f32_16x16x128_f8f6f4 v[134:137], v[122:127], v[2:7], 0 cbsz:2 blgp:2
	v_mfma_f32_16x16x128_f8f6f4 v[138:141], v[122:127], v[14:19], 0 cbsz:2 blgp:2
	v_mfma_f32_16x16x128_f8f6f4 v[142:145], v[122:127], v[26:31], v[188:191] cbsz:2 blgp:2
	v_mfma_f32_16x16x128_f8f6f4 v[204:207], v[122:127], v[38:43], 0 cbsz:2 blgp:2
	v_mfma_f32_16x16x128_f8f6f4 v[208:211], v[122:127], v[50:55], 0 cbsz:2 blgp:2
	v_mfma_f32_16x16x128_f8f6f4 v[212:215], v[122:127], v[62:67], v[188:191] cbsz:2 blgp:2
	s_waitcnt lgkmcnt(0)
	v_mfma_f32_16x16x128_f8f6f4 v[134:137], v[128:133], v[8:13], v[134:137] cbsz:2 blgp:2
	v_mfma_f32_16x16x128_f8f6f4 v[204:207], v[128:133], v[44:49], v[204:207] cbsz:2 blgp:2
	v_mfma_f32_16x16x128_f8f6f4 v[138:141], v[128:133], v[20:25], v[138:141] cbsz:2 blgp:2
	v_mfma_f32_16x16x128_f8f6f4 v[208:211], v[128:133], v[56:61], v[208:211] cbsz:2 blgp:2
	v_mfma_f32_16x16x128_f8f6f4 v[142:145], v[128:133], v[32:37], v[142:145] cbsz:2 blgp:2
	v_mfma_f32_16x16x128_f8f6f4 v[212:215], v[128:133], v[68:73], v[212:215] cbsz:2 blgp:2
	v_cndmask_b32_e64 v158, v134, v204, s[0:1]
	v_fma_mix_f32 v158, v158, v100, v83 op_sel:[0,0,1] op_sel_hi:[0,0,1]
	v_exp_f32_e32 v158, v158
	v_cndmask_b32_e64 v159, v138, v208, s[0:1]
	v_fma_mix_f32 v159, v159, v101, v75 op_sel:[0,0,1] op_sel_hi:[0,0,1]
	v_exp_f32_e32 v159, v159
	v_fma_f32 v158, v158, v186, v186
	v_rcp_f32_e32 v158, v158
	v_add_f32_e32 v159, 1.0, v159
	v_rcp_f32_e32 v159, v159
	v_cndmask_b32_e64 v160, v142, v212, s[0:1]
	v_fma_mix_f32 v161, v158, v160, v79 op_sel:[0,0,1] op_sel_hi:[0,0,1]
	v_exp_f32_e32 v161, v161
	s_add_u32 s48, s48, s40
	v_add_f32_e32 v161, 1.0, v161
	v_rcp_f32_e32 v161, v161
	s_addc_u32 s49, s49, s41
	v_fma_f32 v162, v161, -2.0, 1.0
	v_sub_f32_e32 v163, v176, v162
	v_fma_f32 v176, v159, v163, v162
	v_fma_f32 v164, |v176|, s17, v113
	v_fma_f32 v165, |v176|, s18, v114
	v_fma_f32 v166, |v176|, s19, v115
	v_lshrrev_b32_e32 v167, 26, v176
	v_min3_u32 v164, v164, v165, v166
	v_bfi_b32 v168, 31, v164, v167
	s_nop 1
	v_mul_u32_u24_dpp v170, v168, v180 quad_perm:[1,2,3,3] row_mask:0xf bank_mask:0xf bound_ctrl:1
	v_mad_u32_u24 v171, v168, v181, v170
	ds_write_b8_d16_hi v184, v171
	global_store_short_d16_hi v185, v176, s[48:49]
	s_waitcnt lgkmcnt(0)
	s_barrier
	ds_read_b64 v[122:123], v105 offset:0
	ds_read_b64 v[124:125], v105 offset:8
	ds_read_b64 v[126:127], v105 offset:16
	s_barrier
	ds_read_b64 v[128:129], v105 offset:96
	ds_read_b64 v[130:131], v105 offset:104
	ds_read_b64 v[132:133], v105 offset:112
	s_waitcnt lgkmcnt(3)
	v_mfma_f32_16x16x128_f8f6f4 v[134:137], v[122:127], v[2:7], 0 cbsz:2 blgp:2
	v_mfma_f32_16x16x128_f8f6f4 v[138:141], v[122:127], v[14:19], 0 cbsz:2 blgp:2
	v_mfma_f32_16x16x128_f8f6f4 v[142:145], v[122:127], v[26:31], v[188:191] cbsz:2 blgp:2
	v_mfma_f32_16x16x128_f8f6f4 v[204:207], v[122:127], v[38:43], 0 cbsz:2 blgp:2
	v_mfma_f32_16x16x128_f8f6f4 v[208:211], v[122:127], v[50:55], 0 cbsz:2 blgp:2
	v_mfma_f32_16x16x128_f8f6f4 v[212:215], v[122:127], v[62:67], v[188:191] cbsz:2 blgp:2
	s_waitcnt lgkmcnt(0)
	v_mfma_f32_16x16x128_f8f6f4 v[134:137], v[128:133], v[8:13], v[134:137] cbsz:2 blgp:2
	v_mfma_f32_16x16x128_f8f6f4 v[204:207], v[128:133], v[44:49], v[204:207] cbsz:2 blgp:2
	v_mfma_f32_16x16x128_f8f6f4 v[138:141], v[128:133], v[20:25], v[138:141] cbsz:2 blgp:2
	v_mfma_f32_16x16x128_f8f6f4 v[208:211], v[128:133], v[56:61], v[208:211] cbsz:2 blgp:2
	v_mfma_f32_16x16x128_f8f6f4 v[142:145], v[128:133], v[32:37], v[142:145] cbsz:2 blgp:2
	v_mfma_f32_16x16x128_f8f6f4 v[212:215], v[128:133], v[68:73], v[212:215] cbsz:2 blgp:2
	v_cndmask_b32_e64 v158, v134, v204, s[0:1]
	v_fma_mix_f32 v158, v158, v100, v84 op_sel_hi:[0,0,1]
	v_exp_f32_e32 v158, v158
	v_cndmask_b32_e64 v159, v138, v208, s[0:1]
	v_fma_mix_f32 v159, v159, v101, v76 op_sel_hi:[0,0,1]
	v_exp_f32_e32 v159, v159
	v_fma_f32 v158, v158, v186, v186
	v_rcp_f32_e32 v158, v158
	v_add_f32_e32 v159, 1.0, v159
	v_rcp_f32_e32 v159, v159
	v_cndmask_b32_e64 v160, v142, v212, s[0:1]
	v_fma_mix_f32 v161, v158, v160, v80 op_sel_hi:[0,0,1]
	v_exp_f32_e32 v161, v161
	s_add_u32 s48, s48, s40
	v_add_f32_e32 v161, 1.0, v161
	v_rcp_f32_e32 v161, v161
	s_addc_u32 s49, s49, s41
	v_fma_f32 v162, v161, -2.0, 1.0
	v_sub_f32_e32 v163, v176, v162
	v_fma_f32 v176, v159, v163, v162
	v_fma_f32 v164, |v176|, s17, v113
	v_fma_f32 v165, |v176|, s18, v114
	v_fma_f32 v166, |v176|, s19, v115
	v_lshrrev_b32_e32 v167, 26, v176
	v_min3_u32 v164, v164, v165, v166
	v_bfi_b32 v168, 31, v164, v167
	s_nop 1
	v_mul_u32_u24_dpp v170, v168, v180 quad_perm:[1,2,3,3] row_mask:0xf bank_mask:0xf bound_ctrl:1
	v_mad_u32_u24 v171, v168, v181, v170
	ds_write_b8_d16_hi v184, v171 offset:416
	global_store_short_d16_hi v185, v176, s[48:49]
	s_waitcnt lgkmcnt(0)
	s_barrier
	ds_read_b64 v[122:123], v105 offset:416
	ds_read_b64 v[124:125], v105 offset:424
	ds_read_b64 v[126:127], v105 offset:432
	s_barrier
	ds_read_b64 v[128:129], v105 offset:512
	ds_read_b64 v[130:131], v105 offset:520
	ds_read_b64 v[132:133], v105 offset:528
	s_waitcnt lgkmcnt(3)
	v_mfma_f32_16x16x128_f8f6f4 v[134:137], v[122:127], v[2:7], 0 cbsz:2 blgp:2
	v_mfma_f32_16x16x128_f8f6f4 v[138:141], v[122:127], v[14:19], 0 cbsz:2 blgp:2
	v_mfma_f32_16x16x128_f8f6f4 v[142:145], v[122:127], v[26:31], v[188:191] cbsz:2 blgp:2
	v_mfma_f32_16x16x128_f8f6f4 v[204:207], v[122:127], v[38:43], 0 cbsz:2 blgp:2
	v_mfma_f32_16x16x128_f8f6f4 v[208:211], v[122:127], v[50:55], 0 cbsz:2 blgp:2
	v_mfma_f32_16x16x128_f8f6f4 v[212:215], v[122:127], v[62:67], v[188:191] cbsz:2 blgp:2
	s_waitcnt lgkmcnt(0)
	v_mfma_f32_16x16x128_f8f6f4 v[134:137], v[128:133], v[8:13], v[134:137] cbsz:2 blgp:2
	v_mfma_f32_16x16x128_f8f6f4 v[204:207], v[128:133], v[44:49], v[204:207] cbsz:2 blgp:2
	v_mfma_f32_16x16x128_f8f6f4 v[138:141], v[128:133], v[20:25], v[138:141] cbsz:2 blgp:2
	v_mfma_f32_16x16x128_f8f6f4 v[208:211], v[128:133], v[56:61], v[208:211] cbsz:2 blgp:2
	v_mfma_f32_16x16x128_f8f6f4 v[142:145], v[128:133], v[32:37], v[142:145] cbsz:2 blgp:2
	v_mfma_f32_16x16x128_f8f6f4 v[212:215], v[128:133], v[68:73], v[212:215] cbsz:2 blgp:2
	v_cndmask_b32_e64 v158, v134, v204, s[0:1]
	v_fma_mix_f32 v158, v158, v100, v84 op_sel:[0,0,1] op_sel_hi:[0,0,1]
	v_exp_f32_e32 v158, v158
	v_cndmask_b32_e64 v159, v138, v208, s[0:1]
	v_fma_mix_f32 v159, v159, v101, v76 op_sel:[0,0,1] op_sel_hi:[0,0,1]
	v_exp_f32_e32 v159, v159
	v_fma_f32 v158, v158, v186, v186
	v_rcp_f32_e32 v158, v158
	v_add_f32_e32 v159, 1.0, v159
	v_rcp_f32_e32 v159, v159
	v_cndmask_b32_e64 v160, v142, v212, s[0:1]
	v_fma_mix_f32 v161, v158, v160, v80 op_sel:[0,0,1] op_sel_hi:[0,0,1]
	v_exp_f32_e32 v161, v161
	s_add_u32 s48, s48, s40
	v_add_f32_e32 v161, 1.0, v161
	v_rcp_f32_e32 v161, v161
	s_addc_u32 s49, s49, s41
	v_fma_f32 v162, v161, -2.0, 1.0
	v_sub_f32_e32 v163, v176, v162
	v_fma_f32 v176, v159, v163, v162
	v_fma_f32 v164, |v176|, s17, v113
	v_fma_f32 v165, |v176|, s18, v114
	v_fma_f32 v166, |v176|, s19, v115
	v_lshrrev_b32_e32 v167, 26, v176
	v_min3_u32 v164, v164, v165, v166
	v_bfi_b32 v168, 31, v164, v167
	s_nop 1
	v_mul_u32_u24_dpp v170, v168, v180 quad_perm:[1,2,3,3] row_mask:0xf bank_mask:0xf bound_ctrl:1
	v_mad_u32_u24 v171, v168, v181, v170
	ds_write_b8_d16_hi v184, v171
	global_store_short_d16_hi v185, v176, s[48:49]
	s_waitcnt lgkmcnt(0)
	s_barrier
	ds_read_b64 v[122:123], v105 offset:0
	ds_read_b64 v[124:125], v105 offset:8
	ds_read_b64 v[126:127], v105 offset:16
	s_barrier
	ds_read_b64 v[128:129], v105 offset:96
	ds_read_b64 v[130:131], v105 offset:104
	ds_read_b64 v[132:133], v105 offset:112
	s_waitcnt lgkmcnt(3)
	v_mfma_f32_16x16x128_f8f6f4 v[134:137], v[122:127], v[2:7], 0 cbsz:2 blgp:2
	v_mfma_f32_16x16x128_f8f6f4 v[138:141], v[122:127], v[14:19], 0 cbsz:2 blgp:2
	v_mfma_f32_16x16x128_f8f6f4 v[142:145], v[122:127], v[26:31], v[188:191] cbsz:2 blgp:2
	v_mfma_f32_16x16x128_f8f6f4 v[204:207], v[122:127], v[38:43], 0 cbsz:2 blgp:2
	v_mfma_f32_16x16x128_f8f6f4 v[208:211], v[122:127], v[50:55], 0 cbsz:2 blgp:2
	v_mfma_f32_16x16x128_f8f6f4 v[212:215], v[122:127], v[62:67], v[188:191] cbsz:2 blgp:2
	s_waitcnt lgkmcnt(0)
	v_mfma_f32_16x16x128_f8f6f4 v[134:137], v[128:133], v[8:13], v[134:137] cbsz:2 blgp:2
	v_mfma_f32_16x16x128_f8f6f4 v[204:207], v[128:133], v[44:49], v[204:207] cbsz:2 blgp:2
	v_mfma_f32_16x16x128_f8f6f4 v[138:141], v[128:133], v[20:25], v[138:141] cbsz:2 blgp:2
	v_mfma_f32_16x16x128_f8f6f4 v[208:211], v[128:133], v[56:61], v[208:211] cbsz:2 blgp:2
	v_mfma_f32_16x16x128_f8f6f4 v[142:145], v[128:133], v[32:37], v[142:145] cbsz:2 blgp:2
	v_mfma_f32_16x16x128_f8f6f4 v[212:215], v[128:133], v[68:73], v[212:215] cbsz:2 blgp:2
	v_cndmask_b32_e64 v158, v134, v204, s[0:1]
	v_fma_mix_f32 v158, v158, v100, v85 op_sel_hi:[0,0,1]
	v_exp_f32_e32 v158, v158
	v_cndmask_b32_e64 v159, v138, v208, s[0:1]
	v_fma_mix_f32 v159, v159, v101, v77 op_sel_hi:[0,0,1]
	v_exp_f32_e32 v159, v159
	v_fma_f32 v158, v158, v186, v186
	v_rcp_f32_e32 v158, v158
	v_add_f32_e32 v159, 1.0, v159
	v_rcp_f32_e32 v159, v159
	v_cndmask_b32_e64 v160, v142, v212, s[0:1]
	v_fma_mix_f32 v161, v158, v160, v81 op_sel_hi:[0,0,1]
	v_exp_f32_e32 v161, v161
	s_add_u32 s48, s48, s40
	v_add_f32_e32 v161, 1.0, v161
	v_rcp_f32_e32 v161, v161
	s_addc_u32 s49, s49, s41
	v_fma_f32 v162, v161, -2.0, 1.0
	v_sub_f32_e32 v163, v176, v162
	v_fma_f32 v176, v159, v163, v162
	v_fma_f32 v164, |v176|, s17, v113
	v_fma_f32 v165, |v176|, s18, v114
	v_fma_f32 v166, |v176|, s19, v115
	v_lshrrev_b32_e32 v167, 26, v176
	v_min3_u32 v164, v164, v165, v166
	v_bfi_b32 v168, 31, v164, v167
	s_nop 1
	v_mul_u32_u24_dpp v170, v168, v180 quad_perm:[1,2,3,3] row_mask:0xf bank_mask:0xf bound_ctrl:1
	v_mad_u32_u24 v171, v168, v181, v170
	ds_write_b8_d16_hi v184, v171 offset:416
	global_store_short_d16_hi v185, v176, s[48:49]
	s_waitcnt lgkmcnt(0)
	s_barrier
	ds_read_b64 v[122:123], v105 offset:416
	ds_read_b64 v[124:125], v105 offset:424
	ds_read_b64 v[126:127], v105 offset:432
	s_barrier
	ds_read_b64 v[128:129], v105 offset:512
	ds_read_b64 v[130:131], v105 offset:520
	ds_read_b64 v[132:133], v105 offset:528
	s_waitcnt lgkmcnt(3)
	v_mfma_f32_16x16x128_f8f6f4 v[134:137], v[122:127], v[2:7], 0 cbsz:2 blgp:2
	v_mfma_f32_16x16x128_f8f6f4 v[138:141], v[122:127], v[14:19], 0 cbsz:2 blgp:2
	v_mfma_f32_16x16x128_f8f6f4 v[142:145], v[122:127], v[26:31], v[188:191] cbsz:2 blgp:2
	v_mfma_f32_16x16x128_f8f6f4 v[204:207], v[122:127], v[38:43], 0 cbsz:2 blgp:2
	v_mfma_f32_16x16x128_f8f6f4 v[208:211], v[122:127], v[50:55], 0 cbsz:2 blgp:2
	v_mfma_f32_16x16x128_f8f6f4 v[212:215], v[122:127], v[62:67], v[188:191] cbsz:2 blgp:2
	s_waitcnt lgkmcnt(0)
	v_mfma_f32_16x16x128_f8f6f4 v[134:137], v[128:133], v[8:13], v[134:137] cbsz:2 blgp:2
	v_mfma_f32_16x16x128_f8f6f4 v[204:207], v[128:133], v[44:49], v[204:207] cbsz:2 blgp:2
	v_mfma_f32_16x16x128_f8f6f4 v[138:141], v[128:133], v[20:25], v[138:141] cbsz:2 blgp:2
	v_mfma_f32_16x16x128_f8f6f4 v[208:211], v[128:133], v[56:61], v[208:211] cbsz:2 blgp:2
	v_mfma_f32_16x16x128_f8f6f4 v[142:145], v[128:133], v[32:37], v[142:145] cbsz:2 blgp:2
	v_mfma_f32_16x16x128_f8f6f4 v[212:215], v[128:133], v[68:73], v[212:215] cbsz:2 blgp:2
	v_cndmask_b32_e64 v158, v134, v204, s[0:1]
	v_fma_mix_f32 v158, v158, v100, v85 op_sel:[0,0,1] op_sel_hi:[0,0,1]
	v_exp_f32_e32 v158, v158
	v_cndmask_b32_e64 v159, v138, v208, s[0:1]
	v_fma_mix_f32 v159, v159, v101, v77 op_sel:[0,0,1] op_sel_hi:[0,0,1]
	v_exp_f32_e32 v159, v159
	v_fma_f32 v158, v158, v186, v186
	v_rcp_f32_e32 v158, v158
	v_add_f32_e32 v159, 1.0, v159
	v_rcp_f32_e32 v159, v159
	v_cndmask_b32_e64 v160, v142, v212, s[0:1]
	v_fma_mix_f32 v161, v158, v160, v81 op_sel:[0,0,1] op_sel_hi:[0,0,1]
	v_exp_f32_e32 v161, v161
	s_add_u32 s48, s48, s40
	v_add_f32_e32 v161, 1.0, v161
	v_rcp_f32_e32 v161, v161
	s_addc_u32 s49, s49, s41
	v_fma_f32 v162, v161, -2.0, 1.0
	v_sub_f32_e32 v163, v176, v162
	v_fma_f32 v176, v159, v163, v162
	v_fma_f32 v164, |v176|, s17, v113
	v_fma_f32 v165, |v176|, s18, v114
	v_fma_f32 v166, |v176|, s19, v115
	v_lshrrev_b32_e32 v167, 26, v176
	v_min3_u32 v164, v164, v165, v166
	v_bfi_b32 v168, 31, v164, v167
	s_nop 1
	v_mul_u32_u24_dpp v170, v168, v180 quad_perm:[1,2,3,3] row_mask:0xf bank_mask:0xf bound_ctrl:1
	v_mad_u32_u24 v171, v168, v181, v170
	ds_write_b8_d16_hi v184, v171
	global_store_short_d16_hi v185, v176, s[48:49]
	s_waitcnt lgkmcnt(0)
	s_barrier
	ds_read_b64 v[122:123], v105 offset:0
	ds_read_b64 v[124:125], v105 offset:8
	ds_read_b64 v[126:127], v105 offset:16
	s_barrier
	ds_read_b64 v[128:129], v105 offset:96
	ds_read_b64 v[130:131], v105 offset:104
	ds_read_b64 v[132:133], v105 offset:112
	s_waitcnt vmcnt(8)
	global_load_dwordx4 v[82:85], v[196:197], off
	global_load_dwordx4 v[74:77], v[196:197], off offset:512
	global_load_dwordx4 v[78:81], v[196:197], off offset:1024
	v_lshl_add_u64 v[196:197], v[196:197], 0, s[42:43]
	s_waitcnt lgkmcnt(3)
	v_mfma_f32_16x16x128_f8f6f4 v[134:137], v[122:127], v[2:7], 0 cbsz:2 blgp:2
	v_mfma_f32_16x16x128_f8f6f4 v[138:141], v[122:127], v[14:19], 0 cbsz:2 blgp:2
	v_mfma_f32_16x16x128_f8f6f4 v[142:145], v[122:127], v[26:31], v[188:191] cbsz:2 blgp:2
	v_mfma_f32_16x16x128_f8f6f4 v[204:207], v[122:127], v[38:43], 0 cbsz:2 blgp:2
	v_mfma_f32_16x16x128_f8f6f4 v[208:211], v[122:127], v[50:55], 0 cbsz:2 blgp:2
	v_mfma_f32_16x16x128_f8f6f4 v[212:215], v[122:127], v[62:67], v[188:191] cbsz:2 blgp:2
	s_waitcnt lgkmcnt(0)
	v_mfma_f32_16x16x128_f8f6f4 v[134:137], v[128:133], v[8:13], v[134:137] cbsz:2 blgp:2
	v_mfma_f32_16x16x128_f8f6f4 v[204:207], v[128:133], v[44:49], v[204:207] cbsz:2 blgp:2
	v_mfma_f32_16x16x128_f8f6f4 v[138:141], v[128:133], v[20:25], v[138:141] cbsz:2 blgp:2
	v_mfma_f32_16x16x128_f8f6f4 v[208:211], v[128:133], v[56:61], v[208:211] cbsz:2 blgp:2
	v_mfma_f32_16x16x128_f8f6f4 v[142:145], v[128:133], v[32:37], v[142:145] cbsz:2 blgp:2
	v_mfma_f32_16x16x128_f8f6f4 v[212:215], v[128:133], v[68:73], v[212:215] cbsz:2 blgp:2
	v_cndmask_b32_e64 v158, v134, v204, s[0:1]
	v_fma_mix_f32 v158, v158, v100, v146 op_sel_hi:[0,0,1]
	v_exp_f32_e32 v158, v158
	v_cndmask_b32_e64 v159, v138, v208, s[0:1]
	v_fma_mix_f32 v159, v159, v101, v150 op_sel_hi:[0,0,1]
	v_exp_f32_e32 v159, v159
	v_fma_f32 v158, v158, v186, v186
	v_rcp_f32_e32 v158, v158
	v_add_f32_e32 v159, 1.0, v159
	v_rcp_f32_e32 v159, v159
	v_cndmask_b32_e64 v160, v142, v212, s[0:1]
	v_fma_mix_f32 v161, v158, v160, v154 op_sel_hi:[0,0,1]
	v_exp_f32_e32 v161, v161
	s_add_u32 s48, s48, s40
	v_add_f32_e32 v161, 1.0, v161
	v_rcp_f32_e32 v161, v161
	s_addc_u32 s49, s49, s41
	v_fma_f32 v162, v161, -2.0, 1.0
	v_sub_f32_e32 v163, v176, v162
	v_fma_f32 v176, v159, v163, v162
	v_fma_f32 v164, |v176|, s17, v113
	v_fma_f32 v165, |v176|, s18, v114
	v_fma_f32 v166, |v176|, s19, v115
	v_lshrrev_b32_e32 v167, 26, v176
	v_min3_u32 v164, v164, v165, v166
	v_bfi_b32 v168, 31, v164, v167
	s_nop 1
	v_mul_u32_u24_dpp v170, v168, v180 quad_perm:[1,2,3,3] row_mask:0xf bank_mask:0xf bound_ctrl:1
	v_mad_u32_u24 v171, v168, v181, v170
	ds_write_b8_d16_hi v184, v171 offset:416
	global_store_short_d16_hi v185, v176, s[48:49]
	s_waitcnt lgkmcnt(0)
	s_barrier
	ds_read_b64 v[122:123], v105 offset:416
	ds_read_b64 v[124:125], v105 offset:424
	ds_read_b64 v[126:127], v105 offset:432
	s_barrier
	ds_read_b64 v[128:129], v105 offset:512
	ds_read_b64 v[130:131], v105 offset:520
	ds_read_b64 v[132:133], v105 offset:528
	s_waitcnt lgkmcnt(3)
	v_mfma_f32_16x16x128_f8f6f4 v[134:137], v[122:127], v[2:7], 0 cbsz:2 blgp:2
	v_mfma_f32_16x16x128_f8f6f4 v[138:141], v[122:127], v[14:19], 0 cbsz:2 blgp:2
	v_mfma_f32_16x16x128_f8f6f4 v[142:145], v[122:127], v[26:31], v[188:191] cbsz:2 blgp:2
	v_mfma_f32_16x16x128_f8f6f4 v[204:207], v[122:127], v[38:43], 0 cbsz:2 blgp:2
	v_mfma_f32_16x16x128_f8f6f4 v[208:211], v[122:127], v[50:55], 0 cbsz:2 blgp:2
	v_mfma_f32_16x16x128_f8f6f4 v[212:215], v[122:127], v[62:67], v[188:191] cbsz:2 blgp:2
	s_waitcnt lgkmcnt(0)
	v_mfma_f32_16x16x128_f8f6f4 v[134:137], v[128:133], v[8:13], v[134:137] cbsz:2 blgp:2
	v_mfma_f32_16x16x128_f8f6f4 v[204:207], v[128:133], v[44:49], v[204:207] cbsz:2 blgp:2
	v_mfma_f32_16x16x128_f8f6f4 v[138:141], v[128:133], v[20:25], v[138:141] cbsz:2 blgp:2
	v_mfma_f32_16x16x128_f8f6f4 v[208:211], v[128:133], v[56:61], v[208:211] cbsz:2 blgp:2
	v_mfma_f32_16x16x128_f8f6f4 v[142:145], v[128:133], v[32:37], v[142:145] cbsz:2 blgp:2
	v_mfma_f32_16x16x128_f8f6f4 v[212:215], v[128:133], v[68:73], v[212:215] cbsz:2 blgp:2
	v_cndmask_b32_e64 v158, v134, v204, s[0:1]
	v_fma_mix_f32 v158, v158, v100, v146 op_sel:[0,0,1] op_sel_hi:[0,0,1]
	v_exp_f32_e32 v158, v158
	v_cndmask_b32_e64 v159, v138, v208, s[0:1]
	v_fma_mix_f32 v159, v159, v101, v150 op_sel:[0,0,1] op_sel_hi:[0,0,1]
	v_exp_f32_e32 v159, v159
	v_fma_f32 v158, v158, v186, v186
	v_rcp_f32_e32 v158, v158
	v_add_f32_e32 v159, 1.0, v159
	v_rcp_f32_e32 v159, v159
	v_cndmask_b32_e64 v160, v142, v212, s[0:1]
	v_fma_mix_f32 v161, v158, v160, v154 op_sel:[0,0,1] op_sel_hi:[0,0,1]
	v_exp_f32_e32 v161, v161
	s_add_u32 s48, s48, s40
	v_add_f32_e32 v161, 1.0, v161
	v_rcp_f32_e32 v161, v161
	s_addc_u32 s49, s49, s41
	v_fma_f32 v162, v161, -2.0, 1.0
	v_sub_f32_e32 v163, v176, v162
	v_fma_f32 v176, v159, v163, v162
	v_fma_f32 v164, |v176|, s17, v113
	v_fma_f32 v165, |v176|, s18, v114
	v_fma_f32 v166, |v176|, s19, v115
	v_lshrrev_b32_e32 v167, 26, v176
	v_min3_u32 v164, v164, v165, v166
	v_bfi_b32 v168, 31, v164, v167
	s_nop 1
	v_mul_u32_u24_dpp v170, v168, v180 quad_perm:[1,2,3,3] row_mask:0xf bank_mask:0xf bound_ctrl:1
	v_mad_u32_u24 v171, v168, v181, v170
	ds_write_b8_d16_hi v184, v171
	global_store_short_d16_hi v185, v176, s[48:49]
	s_waitcnt lgkmcnt(0)
	s_barrier
	ds_read_b64 v[122:123], v105 offset:0
	ds_read_b64 v[124:125], v105 offset:8
	ds_read_b64 v[126:127], v105 offset:16
	s_barrier
	ds_read_b64 v[128:129], v105 offset:96
	ds_read_b64 v[130:131], v105 offset:104
	ds_read_b64 v[132:133], v105 offset:112
	s_waitcnt lgkmcnt(3)
	v_mfma_f32_16x16x128_f8f6f4 v[134:137], v[122:127], v[2:7], 0 cbsz:2 blgp:2
	v_mfma_f32_16x16x128_f8f6f4 v[138:141], v[122:127], v[14:19], 0 cbsz:2 blgp:2
	v_mfma_f32_16x16x128_f8f6f4 v[142:145], v[122:127], v[26:31], v[188:191] cbsz:2 blgp:2
	v_mfma_f32_16x16x128_f8f6f4 v[204:207], v[122:127], v[38:43], 0 cbsz:2 blgp:2
	v_mfma_f32_16x16x128_f8f6f4 v[208:211], v[122:127], v[50:55], 0 cbsz:2 blgp:2
	v_mfma_f32_16x16x128_f8f6f4 v[212:215], v[122:127], v[62:67], v[188:191] cbsz:2 blgp:2
	s_waitcnt lgkmcnt(0)
	v_mfma_f32_16x16x128_f8f6f4 v[134:137], v[128:133], v[8:13], v[134:137] cbsz:2 blgp:2
	v_mfma_f32_16x16x128_f8f6f4 v[204:207], v[128:133], v[44:49], v[204:207] cbsz:2 blgp:2
	v_mfma_f32_16x16x128_f8f6f4 v[138:141], v[128:133], v[20:25], v[138:141] cbsz:2 blgp:2
	v_mfma_f32_16x16x128_f8f6f4 v[208:211], v[128:133], v[56:61], v[208:211] cbsz:2 blgp:2
	v_mfma_f32_16x16x128_f8f6f4 v[142:145], v[128:133], v[32:37], v[142:145] cbsz:2 blgp:2
	v_mfma_f32_16x16x128_f8f6f4 v[212:215], v[128:133], v[68:73], v[212:215] cbsz:2 blgp:2
	v_cndmask_b32_e64 v158, v134, v204, s[0:1]
	v_fma_mix_f32 v158, v158, v100, v147 op_sel_hi:[0,0,1]
	v_exp_f32_e32 v158, v158
	v_cndmask_b32_e64 v159, v138, v208, s[0:1]
	v_fma_mix_f32 v159, v159, v101, v151 op_sel_hi:[0,0,1]
	v_exp_f32_e32 v159, v159
	v_fma_f32 v158, v158, v186, v186
	v_rcp_f32_e32 v158, v158
	v_add_f32_e32 v159, 1.0, v159
	v_rcp_f32_e32 v159, v159
	v_cndmask_b32_e64 v160, v142, v212, s[0:1]
	v_fma_mix_f32 v161, v158, v160, v155 op_sel_hi:[0,0,1]
	v_exp_f32_e32 v161, v161
	s_add_u32 s48, s48, s40
	v_add_f32_e32 v161, 1.0, v161
	v_rcp_f32_e32 v161, v161
	s_addc_u32 s49, s49, s41
	v_fma_f32 v162, v161, -2.0, 1.0
	v_sub_f32_e32 v163, v176, v162
	v_fma_f32 v176, v159, v163, v162
	v_fma_f32 v164, |v176|, s17, v113
	v_fma_f32 v165, |v176|, s18, v114
	v_fma_f32 v166, |v176|, s19, v115
	v_lshrrev_b32_e32 v167, 26, v176
	v_min3_u32 v164, v164, v165, v166
	v_bfi_b32 v168, 31, v164, v167
	s_nop 1
	v_mul_u32_u24_dpp v170, v168, v180 quad_perm:[1,2,3,3] row_mask:0xf bank_mask:0xf bound_ctrl:1
	v_mad_u32_u24 v171, v168, v181, v170
	ds_write_b8_d16_hi v184, v171 offset:416
	global_store_short_d16_hi v185, v176, s[48:49]
	s_waitcnt lgkmcnt(0)
	s_barrier
	ds_read_b64 v[122:123], v105 offset:416
	ds_read_b64 v[124:125], v105 offset:424
	ds_read_b64 v[126:127], v105 offset:432
	s_barrier
	ds_read_b64 v[128:129], v105 offset:512
	ds_read_b64 v[130:131], v105 offset:520
	ds_read_b64 v[132:133], v105 offset:528
	s_waitcnt lgkmcnt(3)
	v_mfma_f32_16x16x128_f8f6f4 v[134:137], v[122:127], v[2:7], 0 cbsz:2 blgp:2
	v_mfma_f32_16x16x128_f8f6f4 v[138:141], v[122:127], v[14:19], 0 cbsz:2 blgp:2
	v_mfma_f32_16x16x128_f8f6f4 v[142:145], v[122:127], v[26:31], v[188:191] cbsz:2 blgp:2
	v_mfma_f32_16x16x128_f8f6f4 v[204:207], v[122:127], v[38:43], 0 cbsz:2 blgp:2
	v_mfma_f32_16x16x128_f8f6f4 v[208:211], v[122:127], v[50:55], 0 cbsz:2 blgp:2
	v_mfma_f32_16x16x128_f8f6f4 v[212:215], v[122:127], v[62:67], v[188:191] cbsz:2 blgp:2
	s_waitcnt lgkmcnt(0)
	v_mfma_f32_16x16x128_f8f6f4 v[134:137], v[128:133], v[8:13], v[134:137] cbsz:2 blgp:2
	v_mfma_f32_16x16x128_f8f6f4 v[204:207], v[128:133], v[44:49], v[204:207] cbsz:2 blgp:2
	v_mfma_f32_16x16x128_f8f6f4 v[138:141], v[128:133], v[20:25], v[138:141] cbsz:2 blgp:2
	v_mfma_f32_16x16x128_f8f6f4 v[208:211], v[128:133], v[56:61], v[208:211] cbsz:2 blgp:2
	v_mfma_f32_16x16x128_f8f6f4 v[142:145], v[128:133], v[32:37], v[142:145] cbsz:2 blgp:2
	v_mfma_f32_16x16x128_f8f6f4 v[212:215], v[128:133], v[68:73], v[212:215] cbsz:2 blgp:2
	v_cndmask_b32_e64 v158, v134, v204, s[0:1]
	v_fma_mix_f32 v158, v158, v100, v147 op_sel:[0,0,1] op_sel_hi:[0,0,1]
	v_exp_f32_e32 v158, v158
	v_cndmask_b32_e64 v159, v138, v208, s[0:1]
	v_fma_mix_f32 v159, v159, v101, v151 op_sel:[0,0,1] op_sel_hi:[0,0,1]
	v_exp_f32_e32 v159, v159
	v_fma_f32 v158, v158, v186, v186
	v_rcp_f32_e32 v158, v158
	v_add_f32_e32 v159, 1.0, v159
	v_rcp_f32_e32 v159, v159
	v_cndmask_b32_e64 v160, v142, v212, s[0:1]
	v_fma_mix_f32 v161, v158, v160, v155 op_sel:[0,0,1] op_sel_hi:[0,0,1]
	v_exp_f32_e32 v161, v161
	s_add_u32 s48, s48, s40
	v_add_f32_e32 v161, 1.0, v161
	v_rcp_f32_e32 v161, v161
	s_addc_u32 s49, s49, s41
	v_fma_f32 v162, v161, -2.0, 1.0
	v_sub_f32_e32 v163, v176, v162
	v_fma_f32 v176, v159, v163, v162
	v_fma_f32 v164, |v176|, s17, v113
	v_fma_f32 v165, |v176|, s18, v114
	v_fma_f32 v166, |v176|, s19, v115
	v_lshrrev_b32_e32 v167, 26, v176
	v_min3_u32 v164, v164, v165, v166
	v_bfi_b32 v168, 31, v164, v167
	s_nop 1
	v_mul_u32_u24_dpp v170, v168, v180 quad_perm:[1,2,3,3] row_mask:0xf bank_mask:0xf bound_ctrl:1
	v_mad_u32_u24 v171, v168, v181, v170
	ds_write_b8_d16_hi v184, v171
	global_store_short_d16_hi v185, v176, s[48:49]
	s_waitcnt lgkmcnt(0)
	s_barrier
	ds_read_b64 v[122:123], v105 offset:0
	ds_read_b64 v[124:125], v105 offset:8
	ds_read_b64 v[126:127], v105 offset:16
	s_barrier
	ds_read_b64 v[128:129], v105 offset:96
	ds_read_b64 v[130:131], v105 offset:104
	ds_read_b64 v[132:133], v105 offset:112
	s_waitcnt lgkmcnt(3)
	v_mfma_f32_16x16x128_f8f6f4 v[134:137], v[122:127], v[2:7], 0 cbsz:2 blgp:2
	v_mfma_f32_16x16x128_f8f6f4 v[138:141], v[122:127], v[14:19], 0 cbsz:2 blgp:2
	v_mfma_f32_16x16x128_f8f6f4 v[142:145], v[122:127], v[26:31], v[188:191] cbsz:2 blgp:2
	v_mfma_f32_16x16x128_f8f6f4 v[204:207], v[122:127], v[38:43], 0 cbsz:2 blgp:2
	v_mfma_f32_16x16x128_f8f6f4 v[208:211], v[122:127], v[50:55], 0 cbsz:2 blgp:2
	v_mfma_f32_16x16x128_f8f6f4 v[212:215], v[122:127], v[62:67], v[188:191] cbsz:2 blgp:2
	s_waitcnt lgkmcnt(0)
	v_mfma_f32_16x16x128_f8f6f4 v[134:137], v[128:133], v[8:13], v[134:137] cbsz:2 blgp:2
	v_mfma_f32_16x16x128_f8f6f4 v[204:207], v[128:133], v[44:49], v[204:207] cbsz:2 blgp:2
	v_mfma_f32_16x16x128_f8f6f4 v[138:141], v[128:133], v[20:25], v[138:141] cbsz:2 blgp:2
	v_mfma_f32_16x16x128_f8f6f4 v[208:211], v[128:133], v[56:61], v[208:211] cbsz:2 blgp:2
	v_mfma_f32_16x16x128_f8f6f4 v[142:145], v[128:133], v[32:37], v[142:145] cbsz:2 blgp:2
	v_mfma_f32_16x16x128_f8f6f4 v[212:215], v[128:133], v[68:73], v[212:215] cbsz:2 blgp:2
	v_cndmask_b32_e64 v158, v134, v204, s[0:1]
	v_fma_mix_f32 v158, v158, v100, v148 op_sel_hi:[0,0,1]
	v_exp_f32_e32 v158, v158
	v_cndmask_b32_e64 v159, v138, v208, s[0:1]
	v_fma_mix_f32 v159, v159, v101, v152 op_sel_hi:[0,0,1]
	v_exp_f32_e32 v159, v159
	v_fma_f32 v158, v158, v186, v186
	v_rcp_f32_e32 v158, v158
	v_add_f32_e32 v159, 1.0, v159
	v_rcp_f32_e32 v159, v159
	v_cndmask_b32_e64 v160, v142, v212, s[0:1]
	v_fma_mix_f32 v161, v158, v160, v156 op_sel_hi:[0,0,1]
	v_exp_f32_e32 v161, v161
	s_add_u32 s48, s48, s40
	v_add_f32_e32 v161, 1.0, v161
	v_rcp_f32_e32 v161, v161
	s_addc_u32 s49, s49, s41
	v_fma_f32 v162, v161, -2.0, 1.0
	v_sub_f32_e32 v163, v176, v162
	v_fma_f32 v176, v159, v163, v162
	v_fma_f32 v164, |v176|, s17, v113
	v_fma_f32 v165, |v176|, s18, v114
	v_fma_f32 v166, |v176|, s19, v115
	v_lshrrev_b32_e32 v167, 26, v176
	v_min3_u32 v164, v164, v165, v166
	v_bfi_b32 v168, 31, v164, v167
	s_nop 1
	v_mul_u32_u24_dpp v170, v168, v180 quad_perm:[1,2,3,3] row_mask:0xf bank_mask:0xf bound_ctrl:1
	v_mad_u32_u24 v171, v168, v181, v170
	ds_write_b8_d16_hi v184, v171 offset:416
	global_store_short_d16_hi v185, v176, s[48:49]
	s_waitcnt lgkmcnt(0)
	s_barrier
	ds_read_b64 v[122:123], v105 offset:416
	ds_read_b64 v[124:125], v105 offset:424
	ds_read_b64 v[126:127], v105 offset:432
	s_barrier
	ds_read_b64 v[128:129], v105 offset:512
	ds_read_b64 v[130:131], v105 offset:520
	ds_read_b64 v[132:133], v105 offset:528
	s_waitcnt lgkmcnt(3)
	v_mfma_f32_16x16x128_f8f6f4 v[134:137], v[122:127], v[2:7], 0 cbsz:2 blgp:2
	v_mfma_f32_16x16x128_f8f6f4 v[138:141], v[122:127], v[14:19], 0 cbsz:2 blgp:2
	v_mfma_f32_16x16x128_f8f6f4 v[142:145], v[122:127], v[26:31], v[188:191] cbsz:2 blgp:2
	v_mfma_f32_16x16x128_f8f6f4 v[204:207], v[122:127], v[38:43], 0 cbsz:2 blgp:2
	v_mfma_f32_16x16x128_f8f6f4 v[208:211], v[122:127], v[50:55], 0 cbsz:2 blgp:2
	v_mfma_f32_16x16x128_f8f6f4 v[212:215], v[122:127], v[62:67], v[188:191] cbsz:2 blgp:2
	s_waitcnt lgkmcnt(0)
	v_mfma_f32_16x16x128_f8f6f4 v[134:137], v[128:133], v[8:13], v[134:137] cbsz:2 blgp:2
	v_mfma_f32_16x16x128_f8f6f4 v[204:207], v[128:133], v[44:49], v[204:207] cbsz:2 blgp:2
	v_mfma_f32_16x16x128_f8f6f4 v[138:141], v[128:133], v[20:25], v[138:141] cbsz:2 blgp:2
	v_mfma_f32_16x16x128_f8f6f4 v[208:211], v[128:133], v[56:61], v[208:211] cbsz:2 blgp:2
	v_mfma_f32_16x16x128_f8f6f4 v[142:145], v[128:133], v[32:37], v[142:145] cbsz:2 blgp:2
	v_mfma_f32_16x16x128_f8f6f4 v[212:215], v[128:133], v[68:73], v[212:215] cbsz:2 blgp:2
	v_cndmask_b32_e64 v158, v134, v204, s[0:1]
	v_fma_mix_f32 v158, v158, v100, v148 op_sel:[0,0,1] op_sel_hi:[0,0,1]
	v_exp_f32_e32 v158, v158
	v_cndmask_b32_e64 v159, v138, v208, s[0:1]
	v_fma_mix_f32 v159, v159, v101, v152 op_sel:[0,0,1] op_sel_hi:[0,0,1]
	v_exp_f32_e32 v159, v159
	v_fma_f32 v158, v158, v186, v186
	v_rcp_f32_e32 v158, v158
	v_add_f32_e32 v159, 1.0, v159
	v_rcp_f32_e32 v159, v159
	v_cndmask_b32_e64 v160, v142, v212, s[0:1]
	v_fma_mix_f32 v161, v158, v160, v156 op_sel:[0,0,1] op_sel_hi:[0,0,1]
	v_exp_f32_e32 v161, v161
	s_add_u32 s48, s48, s40
	v_add_f32_e32 v161, 1.0, v161
	v_rcp_f32_e32 v161, v161
	s_addc_u32 s49, s49, s41
	v_fma_f32 v162, v161, -2.0, 1.0
	v_sub_f32_e32 v163, v176, v162
	v_fma_f32 v176, v159, v163, v162
	v_fma_f32 v164, |v176|, s17, v113
	v_fma_f32 v165, |v176|, s18, v114
	v_fma_f32 v166, |v176|, s19, v115
	v_lshrrev_b32_e32 v167, 26, v176
	v_min3_u32 v164, v164, v165, v166
	v_bfi_b32 v168, 31, v164, v167
	s_nop 1
	v_mul_u32_u24_dpp v170, v168, v180 quad_perm:[1,2,3,3] row_mask:0xf bank_mask:0xf bound_ctrl:1
	v_mad_u32_u24 v171, v168, v181, v170
	ds_write_b8_d16_hi v184, v171
	global_store_short_d16_hi v185, v176, s[48:49]
	s_waitcnt lgkmcnt(0)
	s_barrier
	ds_read_b64 v[122:123], v105 offset:0
	ds_read_b64 v[124:125], v105 offset:8
	ds_read_b64 v[126:127], v105 offset:16
	s_barrier
	ds_read_b64 v[128:129], v105 offset:96
	ds_read_b64 v[130:131], v105 offset:104
	ds_read_b64 v[132:133], v105 offset:112
	s_waitcnt lgkmcnt(3)
	v_mfma_f32_16x16x128_f8f6f4 v[134:137], v[122:127], v[2:7], 0 cbsz:2 blgp:2
	v_mfma_f32_16x16x128_f8f6f4 v[138:141], v[122:127], v[14:19], 0 cbsz:2 blgp:2
	v_mfma_f32_16x16x128_f8f6f4 v[142:145], v[122:127], v[26:31], v[188:191] cbsz:2 blgp:2
	v_mfma_f32_16x16x128_f8f6f4 v[204:207], v[122:127], v[38:43], 0 cbsz:2 blgp:2
	v_mfma_f32_16x16x128_f8f6f4 v[208:211], v[122:127], v[50:55], 0 cbsz:2 blgp:2
	v_mfma_f32_16x16x128_f8f6f4 v[212:215], v[122:127], v[62:67], v[188:191] cbsz:2 blgp:2
	s_waitcnt lgkmcnt(0)
	v_mfma_f32_16x16x128_f8f6f4 v[134:137], v[128:133], v[8:13], v[134:137] cbsz:2 blgp:2
	v_mfma_f32_16x16x128_f8f6f4 v[204:207], v[128:133], v[44:49], v[204:207] cbsz:2 blgp:2
	v_mfma_f32_16x16x128_f8f6f4 v[138:141], v[128:133], v[20:25], v[138:141] cbsz:2 blgp:2
	v_mfma_f32_16x16x128_f8f6f4 v[208:211], v[128:133], v[56:61], v[208:211] cbsz:2 blgp:2
	v_mfma_f32_16x16x128_f8f6f4 v[142:145], v[128:133], v[32:37], v[142:145] cbsz:2 blgp:2
	v_mfma_f32_16x16x128_f8f6f4 v[212:215], v[128:133], v[68:73], v[212:215] cbsz:2 blgp:2
	v_cndmask_b32_e64 v158, v134, v204, s[0:1]
	v_fma_mix_f32 v158, v158, v100, v149 op_sel_hi:[0,0,1]
	v_exp_f32_e32 v158, v158
	v_cndmask_b32_e64 v159, v138, v208, s[0:1]
	v_fma_mix_f32 v159, v159, v101, v153 op_sel_hi:[0,0,1]
	v_exp_f32_e32 v159, v159
	v_fma_f32 v158, v158, v186, v186
	v_rcp_f32_e32 v158, v158
	v_add_f32_e32 v159, 1.0, v159
	v_rcp_f32_e32 v159, v159
	v_cndmask_b32_e64 v160, v142, v212, s[0:1]
	v_fma_mix_f32 v161, v158, v160, v157 op_sel_hi:[0,0,1]
	v_exp_f32_e32 v161, v161
	s_add_u32 s48, s48, s40
	v_add_f32_e32 v161, 1.0, v161
	v_rcp_f32_e32 v161, v161
	s_addc_u32 s49, s49, s41
	v_fma_f32 v162, v161, -2.0, 1.0
	v_sub_f32_e32 v163, v176, v162
	v_fma_f32 v176, v159, v163, v162
	v_fma_f32 v164, |v176|, s17, v113
	v_fma_f32 v165, |v176|, s18, v114
	v_fma_f32 v166, |v176|, s19, v115
	v_lshrrev_b32_e32 v167, 26, v176
	v_min3_u32 v164, v164, v165, v166
	v_bfi_b32 v168, 31, v164, v167
	s_nop 1
	v_mul_u32_u24_dpp v170, v168, v180 quad_perm:[1,2,3,3] row_mask:0xf bank_mask:0xf bound_ctrl:1
	v_mad_u32_u24 v171, v168, v181, v170
	ds_write_b8_d16_hi v184, v171 offset:416
	global_store_short_d16_hi v185, v176, s[48:49]
	s_waitcnt lgkmcnt(0)
	s_barrier
	ds_read_b64 v[122:123], v105 offset:416
	ds_read_b64 v[124:125], v105 offset:424
	ds_read_b64 v[126:127], v105 offset:432
	s_barrier
	ds_read_b64 v[128:129], v105 offset:512
	ds_read_b64 v[130:131], v105 offset:520
	ds_read_b64 v[132:133], v105 offset:528
	s_add_i32 s44, s44, 16
	s_waitcnt lgkmcnt(3)
	v_mfma_f32_16x16x128_f8f6f4 v[134:137], v[122:127], v[2:7], 0 cbsz:2 blgp:2
	v_mfma_f32_16x16x128_f8f6f4 v[138:141], v[122:127], v[14:19], 0 cbsz:2 blgp:2
	v_mfma_f32_16x16x128_f8f6f4 v[142:145], v[122:127], v[26:31], v[188:191] cbsz:2 blgp:2
	v_mfma_f32_16x16x128_f8f6f4 v[204:207], v[122:127], v[38:43], 0 cbsz:2 blgp:2
	v_mfma_f32_16x16x128_f8f6f4 v[208:211], v[122:127], v[50:55], 0 cbsz:2 blgp:2
	v_mfma_f32_16x16x128_f8f6f4 v[212:215], v[122:127], v[62:67], v[188:191] cbsz:2 blgp:2
	s_waitcnt lgkmcnt(0)
	v_mfma_f32_16x16x128_f8f6f4 v[134:137], v[128:133], v[8:13], v[134:137] cbsz:2 blgp:2
	v_mfma_f32_16x16x128_f8f6f4 v[204:207], v[128:133], v[44:49], v[204:207] cbsz:2 blgp:2
	v_mfma_f32_16x16x128_f8f6f4 v[138:141], v[128:133], v[20:25], v[138:141] cbsz:2 blgp:2
	v_mfma_f32_16x16x128_f8f6f4 v[208:211], v[128:133], v[56:61], v[208:211] cbsz:2 blgp:2
	v_mfma_f32_16x16x128_f8f6f4 v[142:145], v[128:133], v[32:37], v[142:145] cbsz:2 blgp:2
	v_mfma_f32_16x16x128_f8f6f4 v[212:215], v[128:133], v[68:73], v[212:215] cbsz:2 blgp:2
	v_cndmask_b32_e64 v158, v134, v204, s[0:1]
	v_fma_mix_f32 v158, v158, v100, v149 op_sel:[0,0,1] op_sel_hi:[0,0,1]
	v_exp_f32_e32 v158, v158
	v_cndmask_b32_e64 v159, v138, v208, s[0:1]
	v_fma_mix_f32 v159, v159, v101, v153 op_sel:[0,0,1] op_sel_hi:[0,0,1]
	v_exp_f32_e32 v159, v159
	v_fma_f32 v158, v158, v186, v186
	v_rcp_f32_e32 v158, v158
	v_add_f32_e32 v159, 1.0, v159
	v_rcp_f32_e32 v159, v159
	v_cndmask_b32_e64 v160, v142, v212, s[0:1]
	v_fma_mix_f32 v161, v158, v160, v157 op_sel:[0,0,1] op_sel_hi:[0,0,1]
	v_exp_f32_e32 v161, v161
	s_add_u32 s48, s48, s40
	v_add_f32_e32 v161, 1.0, v161
	v_rcp_f32_e32 v161, v161
	s_addc_u32 s49, s49, s41
	v_fma_f32 v162, v161, -2.0, 1.0
	v_sub_f32_e32 v163, v176, v162
	v_fma_f32 v176, v159, v163, v162
	v_fma_f32 v164, |v176|, s17, v113
	v_fma_f32 v165, |v176|, s18, v114
	v_fma_f32 v166, |v176|, s19, v115
	v_lshrrev_b32_e32 v167, 26, v176
	v_min3_u32 v164, v164, v165, v166
	v_bfi_b32 v168, 31, v164, v167
	s_nop 1
	v_mul_u32_u24_dpp v170, v168, v180 quad_perm:[1,2,3,3] row_mask:0xf bank_mask:0xf bound_ctrl:1
	v_mad_u32_u24 v171, v168, v181, v170
	ds_write_b8_d16_hi v184, v171
	global_store_short_d16_hi v185, v176, s[48:49]
	s_waitcnt lgkmcnt(0)
	s_barrier
	ds_read_b64 v[122:123], v105 offset:0
	ds_read_b64 v[124:125], v105 offset:8
	ds_read_b64 v[126:127], v105 offset:16
	s_cmp_lt_i32 s44, s45
	s_barrier
	s_cbranch_scc1 .Lscan_loop_a_f2
	s_branch .Lscan_exit_f2
	.p2align 6
